# deferred weight-conversion split: 3400 + 1700 tiles deferred, idle-slot quotas 6/9/8/10
# speedup vs baseline: 1.0092x; 1.0022x over previous
; __device__ __forceinline__ void bt_load(const float* __restrict__ src, int N, int perm, int it, int ntn, f32x4 (&v)[8]) {
;     const int wid = threadIdx.x >> 6, lane = threadIdx.x & 63;
;     const int per = 16 * ntn, z = it / per, r = it % per, kt = r / ntn, nt = r % ntn;
;     const int np = nt * 256 + lane * 4;
;     const int sc = perm ? (nt * 128 + (lane & 31) * 4 + (lane >> 5) * 1024) : np;
;     const float* p = src + (size_t)z * 1024 * N + (size_t)(kt * 64 + wid * 8) * N + sc;
; #pragma unroll
;     for (int i = 0; i < 8; ++i) v[i] = __builtin_nontemporal_load((const f32x4*)(p + (size_t)i * N));
; }
; __device__ __forceinline__ void ph_big_transpose(const float* __restrict__ src, int N, int perm, int batch, bf16* __restrict__ dst, float* tile  , int G, int ndefer) {
;     const int tid = threadIdx.x, wid = tid >> 6, lane = tid & 63, ntn = N / 256, total = batch * 16 * ntn - ndefer;
;     int it = (int)blockIdx.x;
;     if (it >= total) return;
;     f32x4 cur[8], nxt[8], nx2[8];
;     bt_load(src, N, perm, it, ntn, cur);
;     if (it + G < total) bt_load(src, N, perm, it + G, ntn, nxt);
;     for (; it < total; it += G) {
;         const bool more = it + G < total, more2 = it + 2 * G < total;
;         if (more2) bt_load(src, N, perm, it + 2 * G, ntn, nx2);
.LBB0_63:
	s_cmpk_gt_i32 s2, 0x12b7
	s_waitcnt lgkmcnt(0)
	s_barrier
	s_cbranch_scc1 .LBB0_71
	s_ashr_i32 s0, s2, 31
	s_lshr_b32 s0, s0, 25
	s_add_i32 s1, s2, s0
	s_ashr_i32 s0, s1, 7
	s_and_b32 s1, s1, 0xff80
	s_sub_i32 s1, s2, s1
	s_bfe_i32 s4, s1, 0x80000
	s_bfe_u32 s4, s4, 0x3000c
	s_add_i32 s4, s1, s4
	s_bfe_i32 s5, s4, 0x80000
	s_and_b32 s4, s4, 0xf8
	v_lshlrev_b32_e32 v2, 2, v0
	s_sub_i32 s1, s1, s4
	v_and_b32_e32 v2, 0x7c, v2
	v_lshlrev_b32_e32 v3, 5, v0
	s_movk_i32 s4, 0x400
	s_sext_i32_i8 s1, s1
	v_and_or_b32 v99, v3, s4, v2
	v_lshl_add_u32 v2, s1, 7, v99
	s_ashr_i32 s1, s0, 31
	s_lshl_b64 s[0:1], s[0:1], 23
	s_sext_i32_i16 s5, s5
	s_add_u32 s0, s68, s0
	s_addc_u32 s1, s69, s1
	s_lshl_b32 s4, s5, 3
	v_lshrrev_b32_e32 v3, 3, v0
	s_andn2_b32 s4, s4, 63
	v_and_b32_e32 v110, 56, v3
	v_or_b32_e32 v4, s4, v110
	v_ashrrev_i32_e32 v5, 31, v4
	v_lshlrev_b64 v[4:5], 13, v[4:5]
	v_lshl_add_u64 v[4:5], s[0:1], 0, v[4:5]
	v_ashrrev_i32_e32 v3, 31, v2
	v_lshl_add_u64 v[2:3], v[2:3], 2, v[4:5]
	s_movk_i32 s0, 0x2000
	v_add_co_u32_e32 v4, vcc, s0, v2
	s_movk_i32 s1, 0x4000
	s_nop 0
	v_addc_co_u32_e32 v5, vcc, 0, v3, vcc
	global_load_dwordx4 v[38:41], v[2:3], off nt
	global_load_dwordx4 v[34:37], v[4:5], off nt
	v_add_co_u32_e32 v4, vcc, s1, v2
	s_movk_i32 s4, 0x6000
	s_nop 0
	v_addc_co_u32_e32 v5, vcc, 0, v3, vcc
	v_add_co_u32_e32 v6, vcc, s4, v2
	s_mov_b32 s5, 0x8000
	s_nop 0
	v_addc_co_u32_e32 v7, vcc, 0, v3, vcc
	global_load_dwordx4 v[46:49], v[4:5], off nt
	global_load_dwordx4 v[42:45], v[6:7], off nt
	v_add_co_u32_e32 v4, vcc, s5, v2
	s_mov_b32 s6, 0xa000
	s_nop 0
	v_addc_co_u32_e32 v5, vcc, 0, v3, vcc
	v_add_co_u32_e32 v6, vcc, s6, v2
	s_add_i32 s6, s62, s2
	s_nop 0
	v_addc_co_u32_e32 v7, vcc, 0, v3, vcc
	global_load_dwordx4 v[54:57], v[4:5], off nt
	global_load_dwordx4 v[50:53], v[6:7], off nt
	v_add_co_u32_e32 v4, vcc, 0xc000, v2
	s_cmpk_gt_i32 s6, 0x12b7
	s_nop 0
	v_addc_co_u32_e32 v5, vcc, 0, v3, vcc
	v_add_co_u32_e32 v2, vcc, 0xe000, v2
	s_nop 1
	v_addc_co_u32_e32 v3, vcc, 0, v3, vcc
	global_load_dwordx4 v[62:65], v[4:5], off nt
	global_load_dwordx4 v[58:61], v[2:3], off nt
	s_cbranch_scc1 .LBB0_66
	s_ashr_i32 s7, s6, 31
	s_lshr_b32 s7, s7, 25
	s_add_i32 s7, s6, s7
	s_ashr_i32 s8, s7, 7
	s_and_b32 s7, s7, 0xff80
	s_sub_i32 s6, s6, s7
	s_bfe_i32 s7, s6, 0x80000
	s_bfe_u32 s7, s7, 0x3000c
	s_add_i32 s7, s6, s7
	s_bfe_i32 s9, s7, 0x80000
	s_and_b32 s7, s7, 0xf8
	s_sub_i32 s6, s6, s7
	s_sext_i32_i16 s10, s9
	s_sext_i32_i8 s6, s6
	s_ashr_i32 s9, s8, 31
	v_lshl_add_u32 v2, s6, 7, v99
	s_lshl_b64 s[6:7], s[8:9], 23
	s_add_u32 s6, s68, s6
	s_addc_u32 s7, s69, s7
	s_lshl_b32 s8, s10, 3
	s_andn2_b32 s8, s8, 63
	v_or_b32_e32 v4, s8, v110
	v_ashrrev_i32_e32 v5, 31, v4
	v_lshlrev_b64 v[4:5], 13, v[4:5]
	v_lshl_add_u64 v[4:5], s[6:7], 0, v[4:5]
	v_ashrrev_i32_e32 v3, 31, v2
	v_lshl_add_u64 v[26:27], v[2:3], 2, v[4:5]
	v_add_co_u32_e32 v6, vcc, s0, v26
	s_nop 1
	v_addc_co_u32_e32 v7, vcc, 0, v27, vcc
	v_add_co_u32_e32 v10, vcc, s1, v26
	global_load_dwordx4 v[2:5], v[26:27], off nt
	s_nop 0
	global_load_dwordx4 v[6:9], v[6:7], off nt
	v_addc_co_u32_e32 v11, vcc, 0, v27, vcc
	v_add_co_u32_e32 v14, vcc, s4, v26
	s_nop 1
	v_addc_co_u32_e32 v15, vcc, 0, v27, vcc
	v_add_co_u32_e32 v18, vcc, s5, v26
	global_load_dwordx4 v[10:13], v[10:11], off nt
	s_nop 0
	global_load_dwordx4 v[14:17], v[14:15], off nt
	v_addc_co_u32_e32 v19, vcc, 0, v27, vcc
	v_add_co_u32_e32 v22, vcc, 0xa000, v26
	s_nop 1
	v_addc_co_u32_e32 v23, vcc, 0, v27, vcc
	v_add_co_u32_e32 v28, vcc, 0xc000, v26
	global_load_dwordx4 v[18:21], v[18:19], off nt
	s_nop 0
	global_load_dwordx4 v[22:25], v[22:23], off nt
	v_addc_co_u32_e32 v29, vcc, 0, v27, vcc
	v_add_co_u32_e32 v30, vcc, 0xe000, v26
	s_nop 1
	v_addc_co_u32_e32 v31, vcc, 0, v27, vcc
	global_load_dwordx4 v[26:29], v[28:29], off nt
	s_nop 0
	global_load_dwordx4 v[30:33], v[30:31], off nt

; __device__ __forceinline__ unsigned g8_cvt_pk(float lo, float hi) { unsigned r; asm volatile("v_cvt_pk_bf16_f32 %0, %1, %2" : "=v"(r) : "v"(lo), "v"(hi)); return r; }
; __device__ __forceinline__ void ph_big_transpose(const float* __restrict__ src, int N, int perm, int batch, bf16* __restrict__ dst, float* tile  , int G, int ndefer) {
;     ...
;     for (; it < total; it += G) {
;         const bool more = it + G < total, more2 = it + 2 * G < total;
;         if (more2) bt_load(src, N, perm, it + 2 * G, ntn, nx2);
;         __syncthreads();
; #pragma unroll
;         for (int i = 0; i < 8; ++i) { float* t = tile + (wid * 8 + i) * 257 + lane * 4; t[0] = cur[i][0]; t[1] = cur[i][1]; t[2] = cur[i][2]; t[3] = cur[i][3]; }
;         __syncthreads();
;         const int per = 16 * ntn, z = it / per, r = it % per, kt = r / ntn, nt = r % ntn;
;         bf16* d = dst + (size_t)z * N * 1024 + (((size_t)nt * 16 + kt) << 14);
;         const int kc = lane & 7;
; #pragma unroll
;         for (int pss = 0; pss < 4; ++pss) {
;             const int n = wid * 32 + pss * 8 + (lane >> 3); float f[8];
; #pragma unroll
;             for (int j = 0; j < 8; ++j) f[j] = tile[(kc * 8 + j) * 257 + n];
;             u32x4 w; w.x = g8_cvt_pk(f[0], f[1]); w.y = g8_cvt_pk(f[2], f[3]); w.z = g8_cvt_pk(f[4], f[5]); w.w = g8_cvt_pk(f[6], f[7]);
;             __builtin_nontemporal_store(w, (u32x4*)(d + n * 64 + kc * 8));
;         }
;         if (more) {
; #pragma unroll
;             for (int i = 0; i < 8; ++i) { cur[i] = nxt[i]; nxt[i] = nx2[i]; } }
;     }
.LBB0_67:
	s_barrier
	s_waitcnt vmcnt(7)
	ds_write_b128 v111, v[38:41]
	v_add_u32_e32 v38, 0x404, v111
	s_ashr_i32 s9, s8, 31
	s_waitcnt vmcnt(6)
	ds_write2_b32 v38, v34, v35 offset1:1
	v_add_u32_e32 v34, 0x40c, v111
	s_lshr_b32 s9, s9, 25
	ds_write2_b32 v34, v36, v37 offset1:1
	v_add_u32_e32 v34, 0x808, v111
	s_add_i32 s9, s8, s9
	s_waitcnt vmcnt(5)
	ds_write2_b64 v34, v[46:47], v[48:49] offset1:1
	v_add_u32_e32 v34, 0xc0c, v111
	s_ashr_i32 s10, s9, 7
	s_and_b32 s9, s9, 0xff80
	s_waitcnt vmcnt(4)
	ds_write2_b32 v34, v42, v43 offset1:1
	v_add_u32_e32 v34, 0xc14, v111
	s_sub_i32 s9, s8, s9
	s_add_i32 s31, s8, s62
	ds_write2_b32 v34, v44, v45 offset1:1
	s_waitcnt vmcnt(3)
	ds_write_b128 v111, v[54:57] offset:4112
	v_add_u32_e32 v34, 0x1414, v111
	s_bfe_i32 s8, s9, 0x80000
	s_waitcnt vmcnt(2)
	ds_write2_b32 v34, v50, v51 offset1:1
	v_add_u32_e32 v34, 0x141c, v111
	s_bfe_u32 s8, s8, 0x3000c
	ds_write2_b32 v34, v52, v53 offset1:1
	v_add_u32_e32 v34, 0x1818, v111
	s_add_i32 s11, s9, s8
	s_waitcnt vmcnt(1)
	ds_write2_b64 v34, v[62:63], v[64:65] offset1:1
	v_add_u32_e32 v34, 0x1c1c, v111
	s_bfe_i32 s8, s11, 0x80000
	s_and_b32 s11, s11, 0xf8
	s_waitcnt vmcnt(0)
	ds_write2_b32 v34, v58, v59 offset1:1
	v_add_u32_e32 v34, 0x1c24, v111
	s_sext_i32_i16 s8, s8
	s_sub_i32 s30, s9, s11
	s_ashr_i32 s11, s10, 31
	ds_write2_b32 v34, v60, v61 offset1:1
	s_waitcnt lgkmcnt(0)
	s_barrier
	s_lshr_b32 s8, s8, 3
	s_lshl_b64 s[10:11], s[10:11], 22
	ds_read_b32 v34, v112 offset:1028
	ds_read_b32 v35, v112 offset:3084
	ds_read_b32 v36, v112 offset:5140
	ds_read_b32 v37, v112 offset:7196
	ds_read_b32 v38, v112 offset:6168
	ds_read_b32 v39, v112 offset:4112
	ds_read_b32 v40, v112 offset:2056
	ds_read_b32 v41, v112
	s_add_u32 s33, s5, s10
	s_addc_u32 s34, s6, s11
	s_bfe_i64 s[10:11], s[30:31], 0x80000
	s_bfe_i64 s[8:9], s[8:9], 0x100000
	s_lshl_b64 s[10:11], s[10:11], 19
	s_add_u32 s10, s33, s10
	s_addc_u32 s11, s34, s11
	s_lshl_b64 s[8:9], s[8:9], 15
	s_waitcnt lgkmcnt(0)
	v_cvt_pk_bf16_f32 v34, v41, v34
	v_cvt_pk_bf16_f32 v35, v40, v35
	v_cvt_pk_bf16_f32 v36, v39, v36
	v_cvt_pk_bf16_f32 v37, v38, v37
	ds_read_b32 v42, v112 offset:1060
	ds_read_b32 v43, v112 offset:3116
	ds_read_b32 v44, v112 offset:5172
	ds_read_b32 v45, v112 offset:7228
	ds_read_b32 v46, v112 offset:6200
	ds_read_b32 v47, v112 offset:4144
	ds_read_b32 v48, v112 offset:2088
	ds_read_b32 v49, v112 offset:32
	s_add_u32 s8, s10, s8
	s_addc_u32 s9, s11, s9
	v_lshl_add_u64 v[38:39], s[8:9], 0, v[100:101]
	v_mov_b32_e32 v103, v101
	v_lshl_add_u64 v[40:41], v[38:39], 0, v[102:103]
	global_store_dwordx4 v[40:41], v[34:37], off nt
	v_mov_b32_e32 v105, v101
	v_lshl_add_u64 v[40:41], v[38:39], 0, v[104:105]
	s_waitcnt lgkmcnt(0)
	v_cvt_pk_bf16_f32 v34, v49, v42
	v_cvt_pk_bf16_f32 v35, v48, v43
	v_cvt_pk_bf16_f32 v36, v47, v44
	v_cvt_pk_bf16_f32 v37, v46, v45
	ds_read_b32 v42, v112 offset:1092
	ds_read_b32 v43, v112 offset:3148
	ds_read_b32 v44, v112 offset:5204
	ds_read_b32 v45, v112 offset:6232
	ds_read_b32 v46, v112 offset:4176
	ds_read_b32 v47, v112 offset:2120
	ds_read_b32 v48, v112 offset:64
	ds_read_b32 v49, v112 offset:7260
	global_store_dwordx4 v[40:41], v[34:37], off nt
	v_mov_b32_e32 v107, v101
	v_lshl_add_u64 v[40:41], v[38:39], 0, v[106:107]
	s_waitcnt lgkmcnt(1)
	v_cvt_pk_bf16_f32 v34, v48, v42
	v_cvt_pk_bf16_f32 v35, v47, v43
	v_cvt_pk_bf16_f32 v36, v46, v44
	s_waitcnt lgkmcnt(0)
	v_cvt_pk_bf16_f32 v37, v45, v49
	ds_read_b32 v42, v112 offset:1124
	ds_read_b32 v43, v112 offset:3180
	ds_read_b32 v44, v112 offset:5236
	ds_read_b32 v45, v112 offset:6264
	ds_read_b32 v46, v112 offset:4208
	ds_read_b32 v47, v112 offset:2152
	ds_read_b32 v48, v112 offset:96
	ds_read_b32 v49, v112 offset:7292
	v_mov_b32_e32 v109, v101
	global_store_dwordx4 v[40:41], v[34:37], off nt
	v_lshl_add_u64 v[38:39], v[38:39], 0, v[108:109]
	v_mov_b64_e32 v[60:61], v[32:33]
	s_waitcnt lgkmcnt(1)
	v_cvt_pk_bf16_f32 v34, v48, v42
	v_cvt_pk_bf16_f32 v35, v47, v43
	v_cvt_pk_bf16_f32 v36, v46, v44
	s_waitcnt lgkmcnt(0)
	v_cvt_pk_bf16_f32 v37, v45, v49
	global_store_dwordx4 v[38:39], v[34:37], off nt
	v_mov_b64_e32 v[64:65], v[28:29]
	v_mov_b64_e32 v[52:53], v[24:25]
	v_mov_b64_e32 v[56:57], v[20:21]
	v_mov_b64_e32 v[44:45], v[16:17]
	v_mov_b64_e32 v[48:49], v[12:13]
	v_mov_b64_e32 v[36:37], v[8:9]
	v_mov_b64_e32 v[40:41], v[4:5]
	v_mov_b64_e32 v[58:59], v[30:31]
	v_mov_b64_e32 v[62:63], v[26:27]
	v_mov_b64_e32 v[50:51], v[22:23]
	v_mov_b64_e32 v[54:55], v[18:19]
	v_mov_b64_e32 v[42:43], v[14:15]
	v_mov_b64_e32 v[46:47], v[10:11]
	v_mov_b64_e32 v[34:35], v[6:7]
	v_mov_b64_e32 v[38:39], v[2:3]
	v_mov_b64_e32 v[30:31], v[94:95]
	v_mov_b64_e32 v[26:27], v[90:91]
	v_mov_b64_e32 v[22:23], v[86:87]
	v_mov_b64_e32 v[18:19], v[82:83]
	v_mov_b64_e32 v[14:15], v[78:79]
	v_mov_b64_e32 v[10:11], v[74:75]
	v_mov_b64_e32 v[6:7], v[70:71]
	v_mov_b64_e32 v[2:3], v[66:67]
	s_cmpk_lt_i32 s31, 0x12b8
	v_mov_b64_e32 v[32:33], v[96:97]
	v_mov_b64_e32 v[28:29], v[92:93]
	v_mov_b64_e32 v[24:25], v[88:89]
	v_mov_b64_e32 v[20:21], v[84:85]
	v_mov_b64_e32 v[16:17], v[80:81]
	v_mov_b64_e32 v[12:13], v[76:77]
	v_mov_b64_e32 v[8:9], v[72:73]
	v_mov_b64_e32 v[4:5], v[68:69]
	s_mov_b32 s8, s31
	s_cbranch_scc0 .LBB0_70
; __device__ __forceinline__ void bt_load(const float* __restrict__ src, int N, int perm, int it, int ntn, f32x4 (&v)[8]) {
;     const int wid = threadIdx.x >> 6, lane = threadIdx.x & 63;
;     const int per = 16 * ntn, z = it / per, r = it % per, kt = r / ntn, nt = r % ntn;
;     const int np = nt * 256 + lane * 4;
;     const int sc = perm ? (nt * 128 + (lane & 31) * 4 + (lane >> 5) * 1024) : np;
;     const float* p = src + (size_t)z * 1024 * N + (size_t)(kt * 64 + wid * 8) * N + sc;
; #pragma unroll
;     for (int i = 0; i < 8; ++i) v[i] = __builtin_nontemporal_load((const f32x4*)(p + (size_t)i * N));
; }
; __device__ __forceinline__ void ph_big_transpose(const float* __restrict__ src, int N, int perm, int batch, bf16* __restrict__ dst, float* tile  , int G, int ndefer) {
;     ...
;     for (; it < total; it += G) {
;         const bool more = it + G < total, more2 = it + 2 * G < total;
;         if (more2) bt_load(src, N, perm, it + 2 * G, ntn, nx2);
.LBB0_68:
	s_add_i32 s9, s7, s8
	s_cmpk_gt_i32 s9, 0x12b7
	s_cbranch_scc1 .LBB0_67
	s_ashr_i32 s10, s9, 31
	s_lshr_b32 s10, s10, 25
	s_add_i32 s11, s9, s10
	s_ashr_i32 s10, s11, 7
	s_and_b32 s11, s11, 0xff80
	s_sub_i32 s9, s9, s11
	s_bfe_i32 s11, s9, 0x80000
	s_bfe_u32 s11, s11, 0x3000c
	s_add_i32 s11, s9, s11
	s_bfe_i32 s30, s11, 0x80000
	s_and_b32 s11, s11, 0xf8
	s_sub_i32 s9, s9, s11
	s_ashr_i32 s11, s10, 31
	s_lshl_b64 s[10:11], s[10:11], 23
	s_sext_i32_i16 s30, s30
	s_sext_i32_i8 s9, s9
	s_add_u32 s10, s68, s10
	v_lshl_add_u32 v66, s9, 7, v99
	s_addc_u32 s11, s69, s11
	s_lshl_b32 s9, s30, 3
	s_andn2_b32 s9, s9, 63
	v_or_b32_e32 v68, s9, v110
	v_ashrrev_i32_e32 v69, 31, v68
	v_lshlrev_b64 v[68:69], 13, v[68:69]
	v_lshl_add_u64 v[68:69], s[10:11], 0, v[68:69]
	v_ashrrev_i32_e32 v67, 31, v66
	v_lshl_add_u64 v[90:91], v[66:67], 2, v[68:69]
	v_add_co_u32_e32 v70, vcc, s0, v90
	s_nop 1
	v_addc_co_u32_e32 v71, vcc, 0, v91, vcc
	v_add_co_u32_e32 v74, vcc, s1, v90
	global_load_dwordx4 v[66:69], v[90:91], off nt
	s_nop 0
	global_load_dwordx4 v[70:73], v[70:71], off nt
	v_addc_co_u32_e32 v75, vcc, 0, v91, vcc
	v_add_co_u32_e32 v78, vcc, s4, v90
	s_nop 1
	v_addc_co_u32_e32 v79, vcc, 0, v91, vcc
	v_add_co_u32_e32 v82, vcc, 0x8000, v90
	global_load_dwordx4 v[74:77], v[74:75], off nt
	s_nop 0
	global_load_dwordx4 v[78:81], v[78:79], off nt
	v_addc_co_u32_e32 v83, vcc, 0, v91, vcc
	v_add_co_u32_e32 v86, vcc, 0xa000, v90
	s_nop 1
	v_addc_co_u32_e32 v87, vcc, 0, v91, vcc
	v_add_co_u32_e32 v92, vcc, 0xc000, v90
	global_load_dwordx4 v[82:85], v[82:83], off nt
	s_nop 0
	global_load_dwordx4 v[86:89], v[86:87], off nt
	v_addc_co_u32_e32 v93, vcc, 0, v91, vcc
	v_add_co_u32_e32 v94, vcc, 0xe000, v90
	s_nop 1
	v_addc_co_u32_e32 v95, vcc, 0, v91, vcc
	global_load_dwordx4 v[90:93], v[92:93], off nt
	s_nop 0
	global_load_dwordx4 v[94:97], v[94:95], off nt
	s_branch .LBB0_67

; __device__ __forceinline__ void bt_load(const float* __restrict__ src, int N, int perm, int it, int ntn, f32x4 (&v)[8]) {
;     const int wid = threadIdx.x >> 6, lane = threadIdx.x & 63;
;     const int per = 16 * ntn, z = it / per, r = it % per, kt = r / ntn, nt = r % ntn;
;     const int np = nt * 256 + lane * 4;
;     const int sc = perm ? (nt * 128 + (lane & 31) * 4 + (lane >> 5) * 1024) : np;
;     const float* p = src + (size_t)z * 1024 * N + (size_t)(kt * 64 + wid * 8) * N + sc;
; #pragma unroll
;     for (int i = 0; i < 8; ++i) v[i] = __builtin_nontemporal_load((const f32x4*)(p + (size_t)i * N));
; }
; __device__ __forceinline__ void ph_big_transpose(const float* __restrict__ src, int N, int perm, int batch, bf16* __restrict__ dst, float* tile  , int G, int ndefer) {
;     const int tid = threadIdx.x, wid = tid >> 6, lane = tid & 63, ntn = N / 256, total = batch * 16 * ntn - ndefer;
;     int it = (int)blockIdx.x;
;     if (it >= total) return;
;     f32x4 cur[8], nxt[8], nx2[8];
;     bt_load(src, N, perm, it, ntn, cur);
;     if (it + G < total) bt_load(src, N, perm, it + G, ntn, nxt);
;     for (; it < total; it += G) {
;         const bool more = it + G < total, more2 = it + 2 * G < total;
;         if (more2) bt_load(src, N, perm, it + 2 * G, ntn, nx2);
.LBB0_71:
	s_cmpk_gt_i32 s2, 0x95b
	s_cbranch_scc1 .LBB0_79
	s_ashr_i32 s0, s2, 31
	s_lshr_b32 s0, s0, 26
	s_add_i32 s1, s2, s0
	s_ashr_i32 s0, s1, 6
	s_and_b32 s1, s1, 0xffc0
	s_sub_i32 s1, s2, s1
	s_bfe_i32 s4, s1, 0x80000
	s_bfe_u32 s4, s4, 0x2000d
	s_add_i32 s4, s1, s4
	s_bfe_i32 s5, s4, 0x80000
	s_and_b32 s4, s4, 0xfc
	s_sub_i32 s1, s1, s4
	v_lshlrev_b32_e32 v2, 2, v0
	s_sext_i32_i8 s1, s1
	v_and_b32_e32 v99, 0xfc, v2
	v_lshl_or_b32 v2, s1, 8, v99
	s_ashr_i32 s1, s0, 31
	s_lshl_b64 s[0:1], s[0:1], 22
	s_sext_i32_i16 s5, s5
	s_add_u32 s0, s72, s0
	s_addc_u32 s1, s73, s1
	s_lshl_b32 s4, s5, 4
	v_lshrrev_b32_e32 v3, 3, v0
	s_andn2_b32 s4, s4, 63
	v_and_b32_e32 v110, 56, v3
	v_or_b32_e32 v4, s4, v110
	v_ashrrev_i32_e32 v5, 31, v4
	v_lshlrev_b64 v[4:5], 12, v[4:5]
	v_lshl_add_u64 v[4:5], s[0:1], 0, v[4:5]
	v_ashrrev_i32_e32 v3, 31, v2
	v_lshl_add_u64 v[2:3], v[2:3], 2, v[4:5]
	s_movk_i32 s0, 0x2000
	v_add_co_u32_e32 v4, vcc, s0, v2
	s_movk_i32 s4, 0x4000
	s_nop 0
	v_addc_co_u32_e32 v5, vcc, 0, v3, vcc
	global_load_dwordx4 v[42:45], v[4:5], off offset:-4096 nt
	global_load_dwordx4 v[34:37], v[4:5], off nt
	v_add_co_u32_e32 v4, vcc, s4, v2
	s_movk_i32 s1, 0x5000
	s_nop 0
	v_addc_co_u32_e32 v5, vcc, 0, v3, vcc
	global_load_dwordx4 v[46:49], v[4:5], off offset:-4096 nt
	global_load_dwordx4 v[38:41], v[4:5], off nt
	v_add_co_u32_e32 v4, vcc, s1, v2
	s_add_i32 s5, s62, s2
	s_nop 0
	v_addc_co_u32_e32 v5, vcc, 0, v3, vcc
	global_load_dwordx4 v[62:65], v[2:3], off nt
	global_load_dwordx4 v[50:53], v[4:5], off nt
	v_add_co_u32_e32 v4, vcc, 0x6000, v2
	s_cmpk_gt_i32 s5, 0x95b
	s_nop 0
	v_addc_co_u32_e32 v5, vcc, 0, v3, vcc
	v_add_co_u32_e32 v2, vcc, 0x7000, v2
	s_movk_i32 s1, 0x3000
	s_nop 0
	v_addc_co_u32_e32 v3, vcc, 0, v3, vcc
	global_load_dwordx4 v[58:61], v[4:5], off nt
	global_load_dwordx4 v[54:57], v[2:3], off nt
	s_cbranch_scc1 .LBB0_74
	s_ashr_i32 s6, s5, 31
	s_lshr_b32 s6, s6, 26
	s_add_i32 s7, s5, s6
	s_ashr_i32 s6, s7, 6
	s_and_b32 s7, s7, 0xffc0
	s_sub_i32 s5, s5, s7
	s_bfe_i32 s7, s5, 0x80000
	s_bfe_u32 s7, s7, 0x2000d
	s_add_i32 s7, s5, s7
	s_bfe_i32 s8, s7, 0x80000
	s_and_b32 s7, s7, 0xfc
	s_sub_i32 s5, s5, s7
	s_ashr_i32 s7, s6, 31
	s_lshl_b64 s[6:7], s[6:7], 22
	s_sext_i32_i16 s8, s8
	s_sext_i32_i8 s5, s5
	s_add_u32 s6, s72, s6
	v_lshl_or_b32 v2, s5, 8, v99
	s_addc_u32 s7, s73, s7
	s_lshl_b32 s5, s8, 4
	s_andn2_b32 s5, s5, 63
	v_or_b32_e32 v4, s5, v110
	v_ashrrev_i32_e32 v5, 31, v4
	v_lshlrev_b64 v[4:5], 12, v[4:5]
	v_lshl_add_u64 v[4:5], s[6:7], 0, v[4:5]
	v_ashrrev_i32_e32 v3, 31, v2
	v_lshl_add_u64 v[26:27], v[2:3], 2, v[4:5]
	v_add_co_u32_e32 v2, vcc, s0, v26
	s_nop 1
	v_addc_co_u32_e32 v3, vcc, 0, v27, vcc
	v_add_co_u32_e32 v10, vcc, s4, v26
	global_load_dwordx4 v[6:9], v[2:3], off offset:-4096 nt
	s_nop 0
	global_load_dwordx4 v[2:5], v[2:3], off nt
	v_addc_co_u32_e32 v11, vcc, 0, v27, vcc
	v_add_co_u32_e32 v18, vcc, 0x5000, v26
	global_load_dwordx4 v[14:17], v[10:11], off offset:-4096 nt
	s_nop 0
	global_load_dwordx4 v[10:13], v[10:11], off nt
	v_addc_co_u32_e32 v19, vcc, 0, v27, vcc
	v_add_co_u32_e32 v28, vcc, 0x6000, v26
	global_load_dwordx4 v[22:25], v[26:27], off nt
	s_nop 0
	global_load_dwordx4 v[18:21], v[18:19], off nt
	v_addc_co_u32_e32 v29, vcc, 0, v27, vcc
	v_add_co_u32_e32 v30, vcc, 0x7000, v26
	s_nop 1
	v_addc_co_u32_e32 v31, vcc, 0, v27, vcc
	global_load_dwordx4 v[26:29], v[28:29], off nt
	s_nop 0
	global_load_dwordx4 v[30:33], v[30:31], off nt

; __device__ __forceinline__ unsigned g8_cvt_pk(float lo, float hi) { unsigned r; asm volatile("v_cvt_pk_bf16_f32 %0, %1, %2" : "=v"(r) : "v"(lo), "v"(hi)); return r; }
; __device__ __forceinline__ void ph_big_transpose(const float* __restrict__ src, int N, int perm, int batch, bf16* __restrict__ dst, float* tile  , int G, int ndefer) {
;     ...
;     for (; it < total; it += G) {
;         const bool more = it + G < total, more2 = it + 2 * G < total;
;         if (more2) bt_load(src, N, perm, it + 2 * G, ntn, nx2);
;         __syncthreads();
; #pragma unroll
;         for (int i = 0; i < 8; ++i) { float* t = tile + (wid * 8 + i) * 257 + lane * 4; t[0] = cur[i][0]; t[1] = cur[i][1]; t[2] = cur[i][2]; t[3] = cur[i][3]; }
;         __syncthreads();
;         const int per = 16 * ntn, z = it / per, r = it % per, kt = r / ntn, nt = r % ntn;
;         bf16* d = dst + (size_t)z * N * 1024 + (((size_t)nt * 16 + kt) << 14);
;         const int kc = lane & 7;
; #pragma unroll
;         for (int pss = 0; pss < 4; ++pss) {
;             const int n = wid * 32 + pss * 8 + (lane >> 3); float f[8];
; #pragma unroll
;             for (int j = 0; j < 8; ++j) f[j] = tile[(kc * 8 + j) * 257 + n];
;             u32x4 w; w.x = g8_cvt_pk(f[0], f[1]); w.y = g8_cvt_pk(f[2], f[3]); w.z = g8_cvt_pk(f[4], f[5]); w.w = g8_cvt_pk(f[6], f[7]);
;             __builtin_nontemporal_store(w, (u32x4*)(d + n * 64 + kc * 8));
;         }
;         if (more) {
; #pragma unroll
;             for (int i = 0; i < 8; ++i) { cur[i] = nxt[i]; nxt[i] = nx2[i]; } }
;     }
.LBB0_75:
	s_ashr_i32 s8, s3, 31
	s_barrier
	s_waitcnt vmcnt(3)
	ds_write_b128 v111, v[62:65]
	v_add_u32_e32 v62, 0x404, v111
	s_lshr_b32 s8, s8, 26
	ds_write2_b32 v62, v42, v43 offset1:1
	v_add_u32_e32 v42, 0x40c, v111
	s_add_i32 s9, s3, s8
	ds_write2_b32 v42, v44, v45 offset1:1
	v_add_u32_e32 v42, 0x808, v111
	s_ashr_i32 s8, s9, 6
	s_and_b32 s9, s9, 0xffc0
	s_add_i32 s7, s3, s62
	ds_write2_b64 v42, v[34:35], v[36:37] offset1:1
	v_add_u32_e32 v34, 0xc0c, v111
	s_sub_i32 s3, s3, s9
	ds_write2_b32 v34, v46, v47 offset1:1
	v_add_u32_e32 v34, 0xc14, v111
	s_bfe_i32 s9, s3, 0x80000
	ds_write2_b32 v34, v48, v49 offset1:1
	ds_write_b128 v111, v[38:41] offset:4112
	v_add_u32_e32 v34, 0x1414, v111
	s_bfe_u32 s9, s9, 0x2000d
	s_waitcnt vmcnt(2)
	ds_write2_b32 v34, v50, v51 offset1:1
	v_add_u32_e32 v34, 0x141c, v111
	s_add_i32 s9, s3, s9
	ds_write2_b32 v34, v52, v53 offset1:1
	v_add_u32_e32 v34, 0x1818, v111
	s_bfe_i32 s10, s9, 0x80000
	s_and_b32 s9, s9, 0xfc
	s_waitcnt vmcnt(1)
	ds_write2_b64 v34, v[58:59], v[60:61] offset1:1
	v_add_u32_e32 v34, 0x1c1c, v111
	s_sext_i32_i16 s10, s10
	s_sub_i32 s30, s3, s9
	s_ashr_i32 s9, s8, 31
	s_waitcnt vmcnt(0)
	ds_write2_b32 v34, v54, v55 offset1:1
	v_add_u32_e32 v34, 0x1c24, v111
	s_lshr_b32 s10, s10, 2
	s_lshl_b64 s[8:9], s[8:9], 21
	ds_write2_b32 v34, v56, v57 offset1:1
	s_waitcnt lgkmcnt(0)
	s_barrier
	s_add_u32 s3, s4, s8
	ds_read_b32 v34, v112 offset:1028
	ds_read_b32 v35, v112 offset:3084
	ds_read_b32 v36, v112 offset:5140
	ds_read_b32 v37, v112 offset:7196
	ds_read_b32 v38, v112 offset:6168
	ds_read_b32 v39, v112 offset:4112
	ds_read_b32 v40, v112 offset:2056
	ds_read_b32 v41, v112
	s_addc_u32 s31, s5, s9
	s_bfe_i64 s[8:9], s[30:31], 0x80000
	s_bfe_i64 s[10:11], s[10:11], 0x100000
	s_lshl_b64 s[8:9], s[8:9], 19
	s_add_u32 s3, s3, s8
	s_addc_u32 s30, s31, s9
	s_lshl_b64 s[8:9], s[10:11], 15
	s_waitcnt lgkmcnt(0)
	v_cvt_pk_bf16_f32 v34, v41, v34
	v_cvt_pk_bf16_f32 v35, v40, v35
	v_cvt_pk_bf16_f32 v36, v39, v36
	v_cvt_pk_bf16_f32 v37, v38, v37
	ds_read_b32 v42, v112 offset:1060
	ds_read_b32 v43, v112 offset:3116
	ds_read_b32 v44, v112 offset:5172
	ds_read_b32 v45, v112 offset:7228
	ds_read_b32 v46, v112 offset:6200
	ds_read_b32 v47, v112 offset:4144
	ds_read_b32 v48, v112 offset:2088
	ds_read_b32 v49, v112 offset:32
	s_add_u32 s8, s3, s8
	s_addc_u32 s9, s30, s9
	v_lshl_add_u64 v[38:39], s[8:9], 0, v[100:101]
	v_mov_b32_e32 v103, v101
	v_lshl_add_u64 v[40:41], v[38:39], 0, v[102:103]
	global_store_dwordx4 v[40:41], v[34:37], off nt
	v_mov_b32_e32 v105, v101
	v_lshl_add_u64 v[40:41], v[38:39], 0, v[104:105]
	s_waitcnt lgkmcnt(0)
	v_cvt_pk_bf16_f32 v34, v49, v42
	v_cvt_pk_bf16_f32 v35, v48, v43
	v_cvt_pk_bf16_f32 v36, v47, v44
	v_cvt_pk_bf16_f32 v37, v46, v45
	ds_read_b32 v42, v112 offset:1092
	ds_read_b32 v43, v112 offset:3148
	ds_read_b32 v44, v112 offset:5204
	ds_read_b32 v45, v112 offset:6232
	ds_read_b32 v46, v112 offset:4176
	ds_read_b32 v47, v112 offset:2120
	ds_read_b32 v48, v112 offset:64
	ds_read_b32 v49, v112 offset:7260
	global_store_dwordx4 v[40:41], v[34:37], off nt
	v_mov_b32_e32 v107, v101
	v_lshl_add_u64 v[40:41], v[38:39], 0, v[106:107]
	s_waitcnt lgkmcnt(1)
	v_cvt_pk_bf16_f32 v34, v48, v42
	v_cvt_pk_bf16_f32 v35, v47, v43
	v_cvt_pk_bf16_f32 v36, v46, v44
	s_waitcnt lgkmcnt(0)
	v_cvt_pk_bf16_f32 v37, v45, v49
	ds_read_b32 v42, v112 offset:1124
	ds_read_b32 v43, v112 offset:3180
	ds_read_b32 v44, v112 offset:5236
	ds_read_b32 v45, v112 offset:6264
	ds_read_b32 v46, v112 offset:4208
	ds_read_b32 v47, v112 offset:2152
	ds_read_b32 v48, v112 offset:96
	ds_read_b32 v49, v112 offset:7292
	v_mov_b32_e32 v109, v101
	global_store_dwordx4 v[40:41], v[34:37], off nt
	v_lshl_add_u64 v[38:39], v[38:39], 0, v[108:109]
	v_mov_b64_e32 v[56:57], v[32:33]
	s_waitcnt lgkmcnt(1)
	v_cvt_pk_bf16_f32 v34, v48, v42
	v_cvt_pk_bf16_f32 v35, v47, v43
	v_cvt_pk_bf16_f32 v36, v46, v44
	s_waitcnt lgkmcnt(0)
	v_cvt_pk_bf16_f32 v37, v45, v49
	global_store_dwordx4 v[38:39], v[34:37], off nt
	v_mov_b64_e32 v[60:61], v[28:29]
	v_mov_b64_e32 v[52:53], v[20:21]
	v_mov_b64_e32 v[40:41], v[12:13]
	v_mov_b64_e32 v[48:49], v[16:17]
	v_mov_b64_e32 v[36:37], v[4:5]
	v_mov_b64_e32 v[44:45], v[8:9]
	v_mov_b64_e32 v[64:65], v[24:25]
	v_mov_b64_e32 v[54:55], v[30:31]
	v_mov_b64_e32 v[58:59], v[26:27]
	v_mov_b64_e32 v[50:51], v[18:19]
	v_mov_b64_e32 v[38:39], v[10:11]
	v_mov_b64_e32 v[46:47], v[14:15]
	v_mov_b64_e32 v[34:35], v[2:3]
	v_mov_b64_e32 v[42:43], v[6:7]
	v_mov_b64_e32 v[62:63], v[22:23]
	v_mov_b64_e32 v[30:31], v[94:95]
	v_mov_b64_e32 v[26:27], v[90:91]
	v_mov_b64_e32 v[18:19], v[86:87]
	v_mov_b64_e32 v[10:11], v[82:83]
	v_mov_b64_e32 v[14:15], v[74:75]
	v_mov_b64_e32 v[2:3], v[66:67]
	v_mov_b64_e32 v[6:7], v[70:71]
	v_mov_b64_e32 v[22:23], v[78:79]
	s_cmpk_lt_i32 s7, 0x95c
	v_mov_b64_e32 v[32:33], v[96:97]
	v_mov_b64_e32 v[28:29], v[92:93]
	v_mov_b64_e32 v[20:21], v[88:89]
	v_mov_b64_e32 v[12:13], v[84:85]
	v_mov_b64_e32 v[16:17], v[76:77]
	v_mov_b64_e32 v[4:5], v[68:69]
	v_mov_b64_e32 v[8:9], v[72:73]
	v_mov_b64_e32 v[24:25], v[80:81]
	s_mov_b32 s3, s7
	s_cbranch_scc0 .LBB0_78
.LBB0_76:
	s_add_i32 s7, s6, s3
	s_cmpk_gt_i32 s7, 0x95b
	s_cbranch_scc1 .LBB0_75
	s_ashr_i32 s8, s7, 31
	s_lshr_b32 s8, s8, 26
	s_add_i32 s9, s7, s8
	s_ashr_i32 s8, s9, 6
	s_and_b32 s9, s9, 0xffc0
	s_sub_i32 s7, s7, s9
	s_bfe_i32 s9, s7, 0x80000
	s_bfe_u32 s9, s9, 0x2000d
	s_add_i32 s9, s7, s9
	s_bfe_i32 s10, s9, 0x80000
	s_and_b32 s9, s9, 0xfc
	s_sub_i32 s7, s7, s9
	s_ashr_i32 s9, s8, 31
	s_lshl_b64 s[8:9], s[8:9], 22
	s_sext_i32_i16 s10, s10
	s_sext_i32_i8 s7, s7
	s_add_u32 s8, s72, s8
	v_lshl_or_b32 v66, s7, 8, v99
	s_addc_u32 s9, s73, s9
	s_lshl_b32 s7, s10, 4
	s_andn2_b32 s7, s7, 63
	v_or_b32_e32 v68, s7, v110
	v_ashrrev_i32_e32 v69, 31, v68
	v_lshlrev_b64 v[68:69], 12, v[68:69]
	v_lshl_add_u64 v[68:69], s[8:9], 0, v[68:69]
	v_ashrrev_i32_e32 v67, 31, v66
	v_lshl_add_u64 v[90:91], v[66:67], 2, v[68:69]
	v_add_co_u32_e32 v66, vcc, s0, v90
	s_nop 1
	v_addc_co_u32_e32 v67, vcc, 0, v91, vcc
	v_add_co_u32_e32 v74, vcc, s1, v90
	global_load_dwordx4 v[70:73], v[66:67], off offset:-4096 nt
	s_nop 0
	global_load_dwordx4 v[66:69], v[66:67], off nt
	v_addc_co_u32_e32 v75, vcc, 0, v91, vcc
	v_add_co_u32_e32 v82, vcc, 0x4000, v90
	global_load_dwordx4 v[78:81], v[90:91], off nt
	s_nop 0
	global_load_dwordx4 v[74:77], v[74:75], off nt
	v_addc_co_u32_e32 v83, vcc, 0, v91, vcc
	v_add_co_u32_e32 v86, vcc, 0x5000, v90
	s_nop 1
	v_addc_co_u32_e32 v87, vcc, 0, v91, vcc
	v_add_co_u32_e32 v92, vcc, 0x6000, v90
	global_load_dwordx4 v[82:85], v[82:83], off nt
	s_nop 0
	global_load_dwordx4 v[86:89], v[86:87], off nt
	v_addc_co_u32_e32 v93, vcc, 0, v91, vcc
	v_add_co_u32_e32 v94, vcc, 0x7000, v90
	s_nop 1
	v_addc_co_u32_e32 v95, vcc, 0, v91, vcc
	global_load_dwordx4 v[90:93], v[92:93], off nt
	s_nop 0
	global_load_dwordx4 v[94:97], v[94:95], off nt
	s_branch .LBB0_75

; #define SEAM(k) do { if (IN(k) && IN((k) + 1)) xcd_barrier(bar); \
;         if (PROBE_MASK) { const unsigned long long t_ = __builtin_amdgcn_s_memrealtime(); if ((PROBE_MASK >> (k)) & 1u) pr_acc += t_ - pr_t0; pr_t0 = t_; } } while (0)
; __device__ __forceinline__ void convert_deferred(const Ptrs& P, unsigned char* lds, int quota) {
;     const int tid = threadIdx.x, wid = tid >> 6, lane = tid & 63;
;     float* tile = (float*)lds;
;     volatile __attribute__((address_space(3))) int* slot = (volatile __attribute__((address_space(3))) int*)((__attribute__((address_space(3))) unsigned char*)lds + 131072 + 320 + 11000);
;     unsigned* q = (unsigned*)(P.ws + WS_CTL) + CW_DEFQ;
;     for (int n = 0; n < quota; ++n) {
;         __syncthreads();
;         if (tid == 0) *slot = (int)atomicAdd(q, 1u);
;         __syncthreads();
;         const int t = *slot;
;         if (t >= DEF_GU + DEF_DN) break;
;         const bool gu = t < DEF_GU;
;         const float* src = gu ? P.in[34] : P.in[36]; bf16* dst = (bf16*)(P.ws + (gu ? WS_WGU : WS_WDN));
;         const int N = gu ? 2048 : 1024, ntn = N / 256, it = gu ? 2 * NE * 16 * 8 - DEF_GU + t : 2 * NE * 16 * 4 - DEF_DN + (t - DEF_GU);
; __global__ void __launch_bounds__(NT, 2) mega(Args args) {
;     ...
;     if (IN(2)) { g8::DenseOrder S; S.init(H, D, (const bf16*)(ws + WS_WEVIN), D, R, EVEN_IN_P, G, (int)blockIdx.x, 0); g8::EpiStoreBf16 E{Z, EVEN_IN_P};
;         g8::gemm_phase<g8::EpiStoreBf16, g8::DenseOrder, false, true>(LDSP, D, D, S, E);
;         if (IDLE_LAST(68 * 7)) convert_deferred(P, lds, 4); } SEAM(2);
.LBB0_779:
	s_abs_i32 s3, s62
	v_cvt_f32_u32_e32 v2, s3
	s_sub_i32 s4, 0, s3
	s_mov_b32 s5, 0
	v_rcp_iflag_f32_e32 v2, v2
	s_nop 0
	v_mul_f32_e32 v2, 0x4f7ffffe, v2
	v_cvt_u32_f32_e32 v2, v2
	s_nop 0
	v_readfirstlane_b32 s6, v2
	s_mul_i32 s4, s4, s6
	s_mul_hi_u32 s4, s6, s4
	s_add_i32 s6, s6, s4
	s_mul_hi_u32 s4, s6, 0x1dc
	s_mul_i32 s4, s4, s3
	s_sub_i32 s4, 0x1dc, s4
	s_sub_i32 s6, s4, s3
	s_cmp_ge_u32 s4, s3
	s_cselect_b32 s4, s6, s4
	s_sub_i32 s6, s4, s3
	s_cmp_ge_u32 s4, s3
	s_cselect_b32 s3, s6, s4
	s_cmp_eq_u32 s3, 0
	s_cselect_b64 s[6:7], -1, 0
	s_cmp_lt_i32 s2, s3
	s_cselect_b64 s[8:9], -1, 0
	s_or_b64 s[6:7], s[6:7], s[8:9]
	s_and_b64 vcc, exec, s[6:7]
	s_cbranch_vccnz .LBB0_789
	v_and_b32_e32 v2, 0x7c, v155
	v_lshlrev_b32_e32 v3, 5, v0
	s_movk_i32 s3, 0x400
	v_lshrrev_b32_e32 v4, 6, v0
	v_and_or_b32 v12, v3, s3, v2
	v_bfe_u32 v2, v0, 3, 3
	v_lshl_or_b32 v5, v4, 5, v2
	v_lshlrev_b32_e32 v2, 3, v0
	v_lshl_add_u32 v11, v182, 4, 0
	v_and_b32_e32 v2, 56, v2
	v_mul_u32_u24_e32 v16, 0x2020, v4
	v_mov_b32_e32 v3, 0
	v_lshl_add_u32 v27, v5, 2, 0
	v_mul_u32_u24_e32 v28, 0x404, v2
	v_lshlrev_b32_e32 v10, 6, v5
	s_add_i32 s12, 0, 0x22c38
	v_add_u32_e32 v16, v11, v16
	v_and_b32_e32 v13, 0xfc, v155
	v_and_b32_e32 v14, 56, v154
	s_mov_b32 s3, 6
	v_or_b32_e32 v4, 0x200, v10
	v_mov_b32_e32 v5, v3
	v_or_b32_e32 v6, 0x400, v10
	v_mov_b32_e32 v7, v3
	v_or_b32_e32 v8, 0x600, v10
	v_mov_b32_e32 v9, v3
	v_mov_b32_e32 v15, s12
	s_movk_i32 s13, 0x13eb
	s_movk_i32 s14, 0x800
	s_mov_b32 s15, 0x1104e000
	s_movk_i32 s16, -1004
	v_add_u32_e32 v17, 0x404, v16
	v_add_u32_e32 v18, 0x40c, v16
	v_add_u32_e32 v19, 0x808, v16
	v_add_u32_e32 v20, 0xc0c, v16
	v_add_u32_e32 v21, 0xc14, v16
	v_add_u32_e32 v22, 0x1414, v16
	v_add_u32_e32 v23, 0x141c, v16
	v_add_u32_e32 v24, 0x1818, v16
	v_add_u32_e32 v25, 0x1c1c, v16
	v_add_u32_e32 v26, 0x1c24, v16
	v_lshlrev_b32_e32 v2, 1, v2
	v_add_u32_e32 v27, v27, v28
	v_lshlrev_b32_e32 v10, 1, v10
	s_branch .LBB0_782

; __device__ __forceinline__ unsigned g8_cvt_pk(float lo, float hi) { unsigned r; asm volatile("v_cvt_pk_bf16_f32 %0, %1, %2" : "=v"(r) : "v"(lo), "v"(hi)); return r; }
; __device__ __forceinline__ void bt_load(const float* __restrict__ src, int N, int perm, int it, int ntn, f32x4 (&v)[8]) {
;     const int wid = threadIdx.x >> 6, lane = threadIdx.x & 63;
;     const int per = 16 * ntn, z = it / per, r = it % per, kt = r / ntn, nt = r % ntn;
;     const int np = nt * 256 + lane * 4;
;     const int sc = perm ? (nt * 128 + (lane & 31) * 4 + (lane >> 5) * 1024) : np;
;     const float* p = src + (size_t)z * 1024 * N + (size_t)(kt * 64 + wid * 8) * N + sc;
; #pragma unroll
;     for (int i = 0; i < 8; ++i) v[i] = __builtin_nontemporal_load((const f32x4*)(p + (size_t)i * N));
; }
; __device__ __forceinline__ void convert_deferred(const Ptrs& P, unsigned char* lds, int quota) {
;     ...
;         __syncthreads();
;         if (tid == 0) *slot = (int)atomicAdd(q, 1u);
;         __syncthreads();
;         const int t = *slot;
;         if (t >= DEF_GU + DEF_DN) break;
;         const bool gu = t < DEF_GU;
;         const float* src = gu ? P.in[34] : P.in[36]; bf16* dst = (bf16*)(P.ws + (gu ? WS_WGU : WS_WDN));
;         const int N = gu ? 2048 : 1024, ntn = N / 256, it = gu ? 2 * NE * 16 * 8 - DEF_GU + t : 2 * NE * 16 * 4 - DEF_DN + (t - DEF_GU);
;         f32x4 cur[8];
;         bt_load(src, N, gu ? 1 : 0, it, ntn, cur);
; #pragma unroll
;         for (int i = 0; i < 8; ++i) { float* tp = tile + (wid * 8 + i) * 257 + lane * 4; tp[0] = cur[i][0]; tp[1] = cur[i][1]; tp[2] = cur[i][2]; tp[3] = cur[i][3]; }
;         __syncthreads();
;         const int per = 16 * ntn, z = it / per, r = it % per, kt = r / ntn, nt = r % ntn;
;         bf16* d = dst + (size_t)z * N * 1024 + (((size_t)nt * 16 + kt) << 14);
;         const int kc = lane & 7;
; #pragma unroll
;         for (int pss = 0; pss < 4; ++pss) {
;             const int nn = wid * 32 + pss * 8 + (lane >> 3); float f[8];
; #pragma unroll
;             for (int j = 0; j < 8; ++j) f[j] = tile[(kc * 8 + j) * 257 + nn];
;             u32x4 w; w.x = g8_cvt_pk(f[0], f[1]); w.y = g8_cvt_pk(f[2], f[3]); w.z = g8_cvt_pk(f[4], f[5]); w.w = g8_cvt_pk(f[6], f[7]);
;             *(u32x4*)(d + nn * 64 + kc * 8) = w;
;         }
.LBB0_786:
	s_or_b64 exec, exec, s[6:7]
	s_waitcnt lgkmcnt(0)
	s_barrier
	ds_read_b32 v11, v15
	s_mov_b64 s[6:7], -1
	s_waitcnt lgkmcnt(0)
	v_cmp_lt_i32_e32 vcc, s13, v11
	v_readfirstlane_b32 s4, v11
	s_cbranch_vccnz .LBB0_781
	s_cmpk_gt_i32 s4, 0xd47
	s_cselect_b64 vcc, -1, 0
	s_and_b64 s[6:7], vcc, exec
	s_cselect_b32 s6, s15, 0x104e000
	s_cselect_b32 s11, 0x400, s14
	s_cselect_b32 s17, s73, s69
	s_cselect_b32 s20, s72, s68
	s_cselect_b32 s7, s16, 0x12b8
	s_cselect_b32 s18, 20, 21
	s_cselect_b32 s21, 10, 11
	s_add_u32 s26, s78, s6
	s_addc_u32 s27, s79, 0
	s_lshr_b32 s8, s11, 4
	s_abs_i32 s6, s8
	v_cvt_f32_u32_e32 v11, s6
	s_sub_i32 s19, 0, s6
	s_add_i32 s7, s7, s4
	s_abs_i32 s9, s7
	v_rcp_iflag_f32_e32 v11, v11
	s_xor_b32 s4, s7, s8
	s_lshr_b32 s10, s11, 8
	s_ashr_i32 s4, s4, 31
	v_mul_f32_e32 v11, 0x4f7ffffe, v11
	v_cvt_u32_f32_e32 v11, v11
	s_nop 0
	v_readfirstlane_b32 s28, v11
	s_mul_i32 s19, s19, s28
	s_mul_hi_u32 s19, s28, s19
	s_add_i32 s28, s28, s19
	s_mul_hi_u32 s19, s9, s28
	s_mul_i32 s28, s19, s6
	s_sub_i32 s9, s9, s28
	s_add_i32 s28, s19, 1
	s_sub_i32 s29, s9, s6
	s_cmp_ge_u32 s9, s6
	s_cselect_b32 s19, s28, s19
	s_cselect_b32 s9, s29, s9
	s_add_i32 s28, s19, 1
	s_cmp_ge_u32 s9, s6
	s_cselect_b32 s6, s28, s19
	s_xor_b32 s6, s6, s4
	s_sub_i32 s6, s6, s4
	s_sext_i32_i8 s4, s10
	v_cvt_f32_i32_e32 v11, s4
	s_mul_i32 s8, s6, s8
	s_sub_i32 s7, s7, s8
	v_cvt_f32_i32_e32 v28, s7
	v_rcp_iflag_f32_e32 v29, v11
	s_xor_b32 s4, s7, s4
	s_ashr_i32 s4, s4, 30
	s_or_b32 s4, s4, 1
	v_mul_f32_e32 v29, v28, v29
	v_trunc_f32_e32 v29, v29
	v_fma_f32 v28, -v29, v11, v28
	v_cvt_i32_f32_e32 v29, v29
	v_cmp_ge_f32_e64 s[8:9], |v28|, |v11|
	s_and_b64 s[8:9], s[8:9], exec
	s_cselect_b32 s4, s4, 0
	v_readfirstlane_b32 s8, v29
	s_add_i32 s8, s8, s4
	s_mul_i32 s9, s8, s10
	s_sub_i32 s10, s7, s9
	s_sext_i32_i8 s7, s10
	v_lshl_add_u32 v11, s7, 7, v12
	v_lshl_or_b32 v28, s7, 8, v13
	s_ashr_i32 s7, s6, 31
	s_sext_i32_i8 s4, s8
	s_lshl_b64 s[18:19], s[6:7], s18
	v_lshl_or_b32 v30, s4, 6, v14
	s_lshl_b64 s[18:19], s[18:19], 2
	v_ashrrev_i32_e32 v31, 31, v30
	s_add_u32 s18, s20, s18
	v_cndmask_b32_e32 v28, v11, v28, vcc
	s_addc_u32 s19, s17, s19
	v_lshlrev_b64 v[30:31], s21, v[30:31]
	v_lshl_add_u64 v[30:31], v[30:31], 2, s[18:19]
	v_ashrrev_i32_e32 v29, 31, v28
	v_lshl_add_u64 v[52:53], v[28:29], 2, v[30:31]
	s_lshl_b64 s[18:19], 12, s21
	s_lshl_b32 s4, s11, 2
	v_lshl_add_u64 v[40:41], v[52:53], 0, s[18:19]
	s_lshl_b64 s[18:19], 24, s21
	v_lshl_add_u64 v[36:37], v[52:53], 0, s[4:5]
	v_lshl_add_u64 v[44:45], v[52:53], 0, s[18:19]
	s_lshl_b64 s[18:19], 28, s21
	v_lshl_add_u64 v[54:55], v[36:37], 0, s[4:5]
	v_lshl_add_u64 v[48:49], v[52:53], 0, s[18:19]
	s_lshl_b32 s4, s11, 3
	s_lshl_b64 s[18:19], 20, s21
	global_load_dwordx4 v[28:31], v[52:53], off nt
	global_load_dwordx4 v[32:35], v[36:37], off nt
	s_nop 0
	global_load_dwordx4 v[36:39], v[54:55], off nt
	s_nop 0
	global_load_dwordx4 v[40:43], v[40:41], off nt
	v_lshl_add_u64 v[54:55], v[54:55], 0, s[4:5]
	v_lshl_add_u64 v[56:57], v[52:53], 0, s[18:19]
	global_load_dwordx4 v[44:47], v[44:45], off nt
	s_nop 0
	global_load_dwordx4 v[48:51], v[48:49], off nt
	s_nop 0
	global_load_dwordx4 v[52:55], v[54:55], off nt
	s_nop 0
	global_load_dwordx4 v[56:59], v[56:57], off nt
	s_lshl_b64 s[6:7], s[6:7], s21
	s_lshl_b64 s[6:7], s[6:7], 11
	s_add_u32 s4, s26, s6
	s_addc_u32 s11, s27, s7
	s_bfe_i64 s[6:7], s[10:11], 0x80000
	s_bfe_i64 s[8:9], s[8:9], 0x80000
	s_lshl_b64 s[6:7], s[6:7], 19
	s_add_u32 s4, s4, s6
	s_addc_u32 s10, s11, s7
	s_lshl_b64 s[6:7], s[8:9], 15
	s_add_u32 s6, s4, s6
	s_addc_u32 s7, s10, s7
	v_mov_b32_e32 v11, v3
	s_add_i32 s3, s3, -1
	s_cmp_eq_u32 s3, 0
	s_waitcnt vmcnt(7)
	ds_write_b128 v16, v[28:31]
	s_waitcnt vmcnt(6)
	ds_write2_b32 v17, v32, v33 offset1:1
	ds_write2_b32 v18, v34, v35 offset1:1
	s_waitcnt vmcnt(3)
	ds_write2_b64 v24, v[44:45], v[46:47] offset1:1
	s_waitcnt vmcnt(2)
	ds_write2_b32 v25, v48, v49 offset1:1
	ds_write2_b32 v26, v50, v51 offset1:1
	ds_write2_b64 v19, v[36:37], v[38:39] offset1:1
	ds_write2_b32 v20, v40, v41 offset1:1
	ds_write2_b32 v21, v42, v43 offset1:1
	s_waitcnt vmcnt(1)
	ds_write_b128 v16, v[52:55] offset:4112
	s_waitcnt vmcnt(0)
	ds_write2_b32 v22, v56, v57 offset1:1
	ds_write2_b32 v23, v58, v59 offset1:1
	s_waitcnt lgkmcnt(0)
	s_barrier
	ds_read_b32 v28, v27 offset:1028
	ds_read_b32 v29, v27 offset:3084
	ds_read_b32 v30, v27 offset:5140
	ds_read_b32 v31, v27 offset:7196
	ds_read_b32 v32, v27 offset:6168
	ds_read_b32 v33, v27 offset:4112
	ds_read_b32 v34, v27 offset:2056
	ds_read_b32 v35, v27
	s_waitcnt lgkmcnt(0)
	v_cvt_pk_bf16_f32 v28, v35, v28
	v_cvt_pk_bf16_f32 v29, v34, v29
	v_cvt_pk_bf16_f32 v30, v33, v30
	v_cvt_pk_bf16_f32 v31, v32, v31
	ds_read_b32 v36, v27 offset:1060
	ds_read_b32 v37, v27 offset:3116
	ds_read_b32 v38, v27 offset:5172
	ds_read_b32 v39, v27 offset:7228
	ds_read_b32 v40, v27 offset:6200
	ds_read_b32 v41, v27 offset:4144
	ds_read_b32 v42, v27 offset:2088
	ds_read_b32 v43, v27 offset:32
	v_lshl_add_u64 v[32:33], s[6:7], 0, v[2:3]
	v_lshl_add_u64 v[34:35], v[32:33], 0, v[10:11]
	global_store_dwordx4 v[34:35], v[28:31], off
	v_lshl_add_u64 v[34:35], v[4:5], 1, v[32:33]
	s_cselect_b64 s[6:7], -1, 0
	s_waitcnt lgkmcnt(0)
	v_cvt_pk_bf16_f32 v28, v43, v36
	v_cvt_pk_bf16_f32 v29, v42, v37
	v_cvt_pk_bf16_f32 v30, v41, v38
	v_cvt_pk_bf16_f32 v31, v40, v39
	ds_read_b32 v11, v27 offset:1092
	ds_read_b32 v36, v27 offset:3148
	ds_read_b32 v37, v27 offset:6232
	ds_read_b32 v38, v27 offset:4176
	ds_read_b32 v39, v27 offset:2120
	ds_read_b32 v40, v27 offset:64
	ds_read_b32 v41, v27 offset:5204
	ds_read_b32 v42, v27 offset:7260
	global_store_dwordx4 v[34:35], v[28:31], off
	v_lshl_add_u64 v[34:35], v[6:7], 1, v[32:33]
	v_lshl_add_u64 v[32:33], v[8:9], 1, v[32:33]
	s_waitcnt lgkmcnt(2)
	v_cvt_pk_bf16_f32 v28, v40, v11
	v_cvt_pk_bf16_f32 v29, v39, v36
	s_waitcnt lgkmcnt(1)
	v_cvt_pk_bf16_f32 v30, v38, v41
	s_waitcnt lgkmcnt(0)
	v_cvt_pk_bf16_f32 v31, v37, v42
	ds_read_b32 v11, v27 offset:1124
	ds_read_b32 v36, v27 offset:3180
	ds_read_b32 v37, v27 offset:6264
	ds_read_b32 v38, v27 offset:4208
	ds_read_b32 v39, v27 offset:2152
	ds_read_b32 v40, v27 offset:96
	ds_read_b32 v41, v27 offset:5236
	ds_read_b32 v42, v27 offset:7292
	global_store_dwordx4 v[34:35], v[28:31], off
	s_waitcnt lgkmcnt(2)
	s_nop 0
	v_cvt_pk_bf16_f32 v28, v40, v11
	v_cvt_pk_bf16_f32 v29, v39, v36
	s_waitcnt lgkmcnt(1)
	v_cvt_pk_bf16_f32 v30, v38, v41
	s_waitcnt lgkmcnt(0)
	v_cvt_pk_bf16_f32 v31, v37, v42
	global_store_dwordx4 v[32:33], v[28:31], off
	s_branch .LBB0_781

; #define SEAM(k) do { if (IN(k) && IN((k) + 1)) xcd_barrier(bar); \
;         if (PROBE_MASK) { const unsigned long long t_ = __builtin_amdgcn_s_memrealtime(); if ((PROBE_MASK >> (k)) & 1u) pr_acc += t_ - pr_t0; pr_t0 = t_; } } while (0)
; __device__ __forceinline__ void convert_deferred(const Ptrs& P, unsigned char* lds, int quota) {
;     const int tid = threadIdx.x, wid = tid >> 6, lane = tid & 63;
;     float* tile = (float*)lds;
;     volatile __attribute__((address_space(3))) int* slot = (volatile __attribute__((address_space(3))) int*)((__attribute__((address_space(3))) unsigned char*)lds + 131072 + 320 + 11000);
;     unsigned* q = (unsigned*)(P.ws + WS_CTL) + CW_DEFQ;
;     for (int n = 0; n < quota; ++n) {
;         __syncthreads();
;         if (tid == 0) *slot = (int)atomicAdd(q, 1u);
;         __syncthreads();
;         const int t = *slot;
;         if (t >= DEF_GU + DEF_DN) break;
;         const bool gu = t < DEF_GU;
;         const float* src = gu ? P.in[34] : P.in[36]; bf16* dst = (bf16*)(P.ws + (gu ? WS_WGU : WS_WDN));
;         const int N = gu ? 2048 : 1024, ntn = N / 256, it = gu ? 2 * NE * 16 * 8 - DEF_GU + t : 2 * NE * 16 * 4 - DEF_DN + (t - DEF_GU);
; __global__ void __launch_bounds__(NT, 2) mega(Args args) {
;     ...
;         if (IDLE_LAST(68 * 4)) convert_deferred(P, lds, 4); } SEAM(6);
.LBB0_1286:
	s_abs_i32 s3, s62
	v_cvt_f32_u32_e32 v2, s3
	s_sub_i32 s4, 0, s3
	s_mov_b32 s5, 0
	v_rcp_iflag_f32_e32 v2, v2
	s_nop 0
	v_mul_f32_e32 v2, 0x4f7ffffe, v2
	v_cvt_u32_f32_e32 v2, v2
	s_nop 0
	v_readfirstlane_b32 s6, v2
	s_mul_i32 s4, s4, s6
	s_mul_hi_u32 s4, s6, s4
	s_add_i32 s6, s6, s4
	s_mul_hi_u32 s4, s6, 0x110
	s_mul_i32 s4, s4, s3
	s_sub_i32 s4, 0x110, s4
	s_sub_i32 s6, s4, s3
	s_cmp_ge_u32 s4, s3
	s_cselect_b32 s4, s6, s4
	s_sub_i32 s6, s4, s3
	s_cmp_ge_u32 s4, s3
	s_cselect_b32 s3, s6, s4
	s_cmp_eq_u32 s3, 0
	s_cselect_b64 s[6:7], -1, 0
	s_cmp_lt_i32 s2, s3
	s_cselect_b64 s[8:9], -1, 0
	s_or_b64 s[6:7], s[6:7], s[8:9]
	s_and_b64 vcc, exec, s[6:7]
	s_cbranch_vccnz .LBB0_1296
	v_and_b32_e32 v2, 0x7c, v188
	v_lshlrev_b32_e32 v3, 5, v0
	s_movk_i32 s3, 0x400
	v_and_or_b32 v12, v3, s3, v2
	v_bfe_u32 v2, v0, 3, 3
	v_lshl_or_b32 v4, v1, 5, v2
	v_lshlrev_b32_e32 v2, 3, v0
	v_lshl_add_u32 v11, v182, 4, 0
	v_and_b32_e32 v2, 56, v2
	v_mul_u32_u24_e32 v16, 0x2020, v1
	v_mov_b32_e32 v3, 0
	v_lshl_add_u32 v27, v4, 2, 0
	v_mul_u32_u24_e32 v28, 0x404, v2
	v_lshlrev_b32_e32 v10, 6, v4
	s_add_i32 s12, 0, 0x22c38
	v_add_u32_e32 v16, v11, v16
	v_and_b32_e32 v13, 0xfc, v188
	v_and_b32_e32 v14, 56, v185
	s_mov_b32 s3, 9
	v_or_b32_e32 v4, 0x200, v10
	v_mov_b32_e32 v5, v3
	v_or_b32_e32 v6, 0x400, v10
	v_mov_b32_e32 v7, v3
	v_or_b32_e32 v8, 0x600, v10
	v_mov_b32_e32 v9, v3
	v_mov_b32_e32 v15, s12
	s_movk_i32 s13, 0x13eb
	s_movk_i32 s14, 0x800
	s_mov_b32 s15, 0x1104e000
	s_movk_i32 s16, -1004
	v_add_u32_e32 v17, 0x404, v16
	v_add_u32_e32 v18, 0x40c, v16
	v_add_u32_e32 v19, 0x808, v16
	v_add_u32_e32 v20, 0xc0c, v16
	v_add_u32_e32 v21, 0xc14, v16
	v_add_u32_e32 v22, 0x1414, v16
	v_add_u32_e32 v23, 0x141c, v16
	v_add_u32_e32 v24, 0x1818, v16
	v_add_u32_e32 v25, 0x1c1c, v16
	v_add_u32_e32 v26, 0x1c24, v16
	v_lshlrev_b32_e32 v2, 1, v2
	v_add_u32_e32 v27, v27, v28
	v_lshlrev_b32_e32 v10, 1, v10
	s_branch .LBB0_1289

; __device__ __forceinline__ unsigned g8_cvt_pk(float lo, float hi) { unsigned r; asm volatile("v_cvt_pk_bf16_f32 %0, %1, %2" : "=v"(r) : "v"(lo), "v"(hi)); return r; }
; __device__ __forceinline__ void bt_load(const float* __restrict__ src, int N, int perm, int it, int ntn, f32x4 (&v)[8]) {
;     const int wid = threadIdx.x >> 6, lane = threadIdx.x & 63;
;     const int per = 16 * ntn, z = it / per, r = it % per, kt = r / ntn, nt = r % ntn;
;     const int np = nt * 256 + lane * 4;
;     const int sc = perm ? (nt * 128 + (lane & 31) * 4 + (lane >> 5) * 1024) : np;
;     const float* p = src + (size_t)z * 1024 * N + (size_t)(kt * 64 + wid * 8) * N + sc;
; #pragma unroll
;     for (int i = 0; i < 8; ++i) v[i] = __builtin_nontemporal_load((const f32x4*)(p + (size_t)i * N));
; }
; __device__ __forceinline__ void convert_deferred(const Ptrs& P, unsigned char* lds, int quota) {
;     ...
;         __syncthreads();
;         if (tid == 0) *slot = (int)atomicAdd(q, 1u);
;         __syncthreads();
;         const int t = *slot;
;         if (t >= DEF_GU + DEF_DN) break;
;         const bool gu = t < DEF_GU;
;         const float* src = gu ? P.in[34] : P.in[36]; bf16* dst = (bf16*)(P.ws + (gu ? WS_WGU : WS_WDN));
;         const int N = gu ? 2048 : 1024, ntn = N / 256, it = gu ? 2 * NE * 16 * 8 - DEF_GU + t : 2 * NE * 16 * 4 - DEF_DN + (t - DEF_GU);
;         f32x4 cur[8];
;         bt_load(src, N, gu ? 1 : 0, it, ntn, cur);
; #pragma unroll
;         for (int i = 0; i < 8; ++i) { float* tp = tile + (wid * 8 + i) * 257 + lane * 4; tp[0] = cur[i][0]; tp[1] = cur[i][1]; tp[2] = cur[i][2]; tp[3] = cur[i][3]; }
;         __syncthreads();
;         const int per = 16 * ntn, z = it / per, r = it % per, kt = r / ntn, nt = r % ntn;
;         bf16* d = dst + (size_t)z * N * 1024 + (((size_t)nt * 16 + kt) << 14);
;         const int kc = lane & 7;
; #pragma unroll
;         for (int pss = 0; pss < 4; ++pss) {
;             const int nn = wid * 32 + pss * 8 + (lane >> 3); float f[8];
; #pragma unroll
;             for (int j = 0; j < 8; ++j) f[j] = tile[(kc * 8 + j) * 257 + nn];
;             u32x4 w; w.x = g8_cvt_pk(f[0], f[1]); w.y = g8_cvt_pk(f[2], f[3]); w.z = g8_cvt_pk(f[4], f[5]); w.w = g8_cvt_pk(f[6], f[7]);
;             *(u32x4*)(d + nn * 64 + kc * 8) = w;
;         }
.LBB0_1293:
	s_or_b64 exec, exec, s[6:7]
	s_waitcnt lgkmcnt(0)
	s_barrier
	ds_read_b32 v11, v15
	s_mov_b64 s[6:7], -1
	s_waitcnt lgkmcnt(0)
	v_cmp_lt_i32_e32 vcc, s13, v11
	v_readfirstlane_b32 s4, v11
	s_cbranch_vccnz .LBB0_1288
	s_cmpk_gt_i32 s4, 0xd47
	s_cselect_b64 vcc, -1, 0
	s_and_b64 s[6:7], vcc, exec
	s_cselect_b32 s6, s15, 0x104e000
	s_cselect_b32 s11, 0x400, s14
	s_cselect_b32 s17, s73, s69
	s_cselect_b32 s20, s72, s68
	s_cselect_b32 s7, s16, 0x12b8
	s_cselect_b32 s18, 20, 21
	s_cselect_b32 s21, 10, 11
	s_add_u32 s22, s78, s6
	s_addc_u32 s23, s79, 0
	s_lshr_b32 s8, s11, 4
	s_abs_i32 s6, s8
	v_cvt_f32_u32_e32 v11, s6
	s_sub_i32 s19, 0, s6
	s_add_i32 s7, s7, s4
	s_abs_i32 s9, s7
	v_rcp_iflag_f32_e32 v11, v11
	s_xor_b32 s4, s7, s8
	s_lshr_b32 s10, s11, 8
	s_ashr_i32 s4, s4, 31
	v_mul_f32_e32 v11, 0x4f7ffffe, v11
	v_cvt_u32_f32_e32 v11, v11
	s_nop 0
	v_readfirstlane_b32 s24, v11
	s_mul_i32 s19, s19, s24
	s_mul_hi_u32 s19, s24, s19
	s_add_i32 s24, s24, s19
	s_mul_hi_u32 s19, s9, s24
	s_mul_i32 s24, s19, s6
	s_sub_i32 s9, s9, s24
	s_add_i32 s24, s19, 1
	s_sub_i32 s25, s9, s6
	s_cmp_ge_u32 s9, s6
	s_cselect_b32 s19, s24, s19
	s_cselect_b32 s9, s25, s9
	s_add_i32 s24, s19, 1
	s_cmp_ge_u32 s9, s6
	s_cselect_b32 s6, s24, s19
	s_xor_b32 s6, s6, s4
	s_sub_i32 s6, s6, s4
	s_sext_i32_i8 s4, s10
	v_cvt_f32_i32_e32 v11, s4
	s_mul_i32 s8, s6, s8
	s_sub_i32 s7, s7, s8
	v_cvt_f32_i32_e32 v28, s7
	v_rcp_iflag_f32_e32 v29, v11
	s_xor_b32 s4, s7, s4
	s_ashr_i32 s4, s4, 30
	s_or_b32 s4, s4, 1
	v_mul_f32_e32 v29, v28, v29
	v_trunc_f32_e32 v29, v29
	v_fma_f32 v28, -v29, v11, v28
	v_cvt_i32_f32_e32 v29, v29
	v_cmp_ge_f32_e64 s[8:9], |v28|, |v11|
	s_and_b64 s[8:9], s[8:9], exec
	s_cselect_b32 s4, s4, 0
	v_readfirstlane_b32 s8, v29
	s_add_i32 s8, s8, s4
	s_mul_i32 s9, s8, s10
	s_sub_i32 s10, s7, s9
	s_sext_i32_i8 s7, s10
	v_lshl_add_u32 v11, s7, 7, v12
	v_lshl_or_b32 v28, s7, 8, v13
	s_ashr_i32 s7, s6, 31
	s_sext_i32_i8 s4, s8
	s_lshl_b64 s[18:19], s[6:7], s18
	v_lshl_or_b32 v30, s4, 6, v14
	s_lshl_b64 s[18:19], s[18:19], 2
	v_ashrrev_i32_e32 v31, 31, v30
	s_add_u32 s18, s20, s18
	v_cndmask_b32_e32 v28, v11, v28, vcc
	s_addc_u32 s19, s17, s19
	v_lshlrev_b64 v[30:31], s21, v[30:31]
	v_lshl_add_u64 v[30:31], v[30:31], 2, s[18:19]
	v_ashrrev_i32_e32 v29, 31, v28
	v_lshl_add_u64 v[52:53], v[28:29], 2, v[30:31]
	s_lshl_b64 s[18:19], 12, s21
	s_lshl_b32 s4, s11, 2
	v_lshl_add_u64 v[40:41], v[52:53], 0, s[18:19]
	s_lshl_b64 s[18:19], 24, s21
	v_lshl_add_u64 v[36:37], v[52:53], 0, s[4:5]
	v_lshl_add_u64 v[44:45], v[52:53], 0, s[18:19]
	s_lshl_b64 s[18:19], 28, s21
	v_lshl_add_u64 v[54:55], v[36:37], 0, s[4:5]
	v_lshl_add_u64 v[48:49], v[52:53], 0, s[18:19]
	s_lshl_b32 s4, s11, 3
	s_lshl_b64 s[18:19], 20, s21
	global_load_dwordx4 v[28:31], v[52:53], off nt
	global_load_dwordx4 v[32:35], v[36:37], off nt
	s_nop 0
	global_load_dwordx4 v[36:39], v[54:55], off nt
	s_nop 0
	global_load_dwordx4 v[40:43], v[40:41], off nt
	v_lshl_add_u64 v[54:55], v[54:55], 0, s[4:5]
	v_lshl_add_u64 v[56:57], v[52:53], 0, s[18:19]
	global_load_dwordx4 v[44:47], v[44:45], off nt
	s_nop 0
	global_load_dwordx4 v[48:51], v[48:49], off nt
	s_nop 0
	global_load_dwordx4 v[52:55], v[54:55], off nt
	s_nop 0
	global_load_dwordx4 v[56:59], v[56:57], off nt
	s_lshl_b64 s[6:7], s[6:7], s21
	s_lshl_b64 s[6:7], s[6:7], 11
	s_add_u32 s4, s22, s6
	s_addc_u32 s11, s23, s7
	s_bfe_i64 s[6:7], s[10:11], 0x80000
	s_bfe_i64 s[8:9], s[8:9], 0x80000
	s_lshl_b64 s[6:7], s[6:7], 19
	s_add_u32 s4, s4, s6
	s_addc_u32 s10, s11, s7
	s_lshl_b64 s[6:7], s[8:9], 15
	s_add_u32 s6, s4, s6
	s_addc_u32 s7, s10, s7
	v_mov_b32_e32 v11, v3
	s_add_i32 s3, s3, -1
	s_cmp_eq_u32 s3, 0
	s_waitcnt vmcnt(7)
	ds_write_b128 v16, v[28:31]
	s_waitcnt vmcnt(6)
	ds_write2_b32 v17, v32, v33 offset1:1
	ds_write2_b32 v18, v34, v35 offset1:1
	s_waitcnt vmcnt(3)
	ds_write2_b64 v24, v[44:45], v[46:47] offset1:1
	s_waitcnt vmcnt(2)
	ds_write2_b32 v25, v48, v49 offset1:1
	ds_write2_b32 v26, v50, v51 offset1:1
	ds_write2_b64 v19, v[36:37], v[38:39] offset1:1
	ds_write2_b32 v20, v40, v41 offset1:1
	ds_write2_b32 v21, v42, v43 offset1:1
	s_waitcnt vmcnt(1)
	ds_write_b128 v16, v[52:55] offset:4112
	s_waitcnt vmcnt(0)
	ds_write2_b32 v22, v56, v57 offset1:1
	ds_write2_b32 v23, v58, v59 offset1:1
	s_waitcnt lgkmcnt(0)
	s_barrier
	ds_read_b32 v28, v27 offset:1028
	ds_read_b32 v29, v27 offset:3084
	ds_read_b32 v30, v27 offset:5140
	ds_read_b32 v31, v27 offset:7196
	ds_read_b32 v32, v27 offset:6168
	ds_read_b32 v33, v27 offset:4112
	ds_read_b32 v34, v27 offset:2056
	ds_read_b32 v35, v27
	s_waitcnt lgkmcnt(0)
	v_cvt_pk_bf16_f32 v28, v35, v28
	v_cvt_pk_bf16_f32 v29, v34, v29
	v_cvt_pk_bf16_f32 v30, v33, v30
	v_cvt_pk_bf16_f32 v31, v32, v31
	ds_read_b32 v36, v27 offset:1060
	ds_read_b32 v37, v27 offset:3116
	ds_read_b32 v38, v27 offset:5172
	ds_read_b32 v39, v27 offset:7228
	ds_read_b32 v40, v27 offset:6200
	ds_read_b32 v41, v27 offset:4144
	ds_read_b32 v42, v27 offset:2088
	ds_read_b32 v43, v27 offset:32
	v_lshl_add_u64 v[32:33], s[6:7], 0, v[2:3]
	v_lshl_add_u64 v[34:35], v[32:33], 0, v[10:11]
	global_store_dwordx4 v[34:35], v[28:31], off
	v_lshl_add_u64 v[34:35], v[4:5], 1, v[32:33]
	s_cselect_b64 s[6:7], -1, 0
	s_waitcnt lgkmcnt(0)
	v_cvt_pk_bf16_f32 v28, v43, v36
	v_cvt_pk_bf16_f32 v29, v42, v37
	v_cvt_pk_bf16_f32 v30, v41, v38
	v_cvt_pk_bf16_f32 v31, v40, v39
	ds_read_b32 v11, v27 offset:1092
	ds_read_b32 v36, v27 offset:3148
	ds_read_b32 v37, v27 offset:6232
	ds_read_b32 v38, v27 offset:4176
	ds_read_b32 v39, v27 offset:2120
	ds_read_b32 v40, v27 offset:64
	ds_read_b32 v41, v27 offset:5204
	ds_read_b32 v42, v27 offset:7260
	global_store_dwordx4 v[34:35], v[28:31], off
	v_lshl_add_u64 v[34:35], v[6:7], 1, v[32:33]
	v_lshl_add_u64 v[32:33], v[8:9], 1, v[32:33]
	s_waitcnt lgkmcnt(2)
	v_cvt_pk_bf16_f32 v28, v40, v11
	v_cvt_pk_bf16_f32 v29, v39, v36
	s_waitcnt lgkmcnt(1)
	v_cvt_pk_bf16_f32 v30, v38, v41
	s_waitcnt lgkmcnt(0)
	v_cvt_pk_bf16_f32 v31, v37, v42
	ds_read_b32 v11, v27 offset:1124
	ds_read_b32 v36, v27 offset:3180
	ds_read_b32 v37, v27 offset:6264
	ds_read_b32 v38, v27 offset:4208
	ds_read_b32 v39, v27 offset:2152
	ds_read_b32 v40, v27 offset:96
	ds_read_b32 v41, v27 offset:5236
	ds_read_b32 v42, v27 offset:7292
	global_store_dwordx4 v[34:35], v[28:31], off
	s_waitcnt lgkmcnt(2)
	s_nop 0
	v_cvt_pk_bf16_f32 v28, v40, v11
	v_cvt_pk_bf16_f32 v29, v39, v36
	s_waitcnt lgkmcnt(1)
	v_cvt_pk_bf16_f32 v30, v38, v41
	s_waitcnt lgkmcnt(0)
	v_cvt_pk_bf16_f32 v31, v37, v42
	global_store_dwordx4 v[32:33], v[28:31], off
	s_branch .LBB0_1288

; #define LAS __attribute__((address_space(3)))
; #define SEAM(k) do { if (IN(k) && IN((k) + 1)) xcd_barrier(bar); \
;         if (PROBE_MASK) { const unsigned long long t_ = __builtin_amdgcn_s_memrealtime(); if ((PROBE_MASK >> (k)) & 1u) pr_acc += t_ - pr_t0; pr_t0 = t_; } } while (0)
; __device__ __forceinline__ void convert_deferred(const Ptrs& P, unsigned char* lds, int quota) {
;     const int tid = threadIdx.x, wid = tid >> 6, lane = tid & 63;
;     float* tile = (float*)lds;
;     volatile __attribute__((address_space(3))) int* slot = (volatile __attribute__((address_space(3))) int*)((__attribute__((address_space(3))) unsigned char*)lds + 131072 + 320 + 11000);
;     unsigned* q = (unsigned*)(P.ws + WS_CTL) + CW_DEFQ;
;     for (int n = 0; n < quota; ++n) {
;         __syncthreads();
;         if (tid == 0) *slot = (int)atomicAdd(q, 1u);
;         __syncthreads();
;         const int t = *slot;
;         if (t >= DEF_GU + DEF_DN) break;
;         const bool gu = t < DEF_GU;
;         const float* src = gu ? P.in[34] : P.in[36]; bf16* dst = (bf16*)(P.ws + (gu ? WS_WGU : WS_WDN));
;         const int N = gu ? 2048 : 1024, ntn = N / 256, it = gu ? 2 * NE * 16 * 8 - DEF_GU + t : 2 * NE * 16 * 4 - DEF_DN + (t - DEF_GU);
; __global__ void __launch_bounds__(NT, 2) mega(Args args) {
;     ...
;         { const int rem_ = ((LAS int*)(LDSP + MISC_OFF + 256))[96] % G; if (rem_ != 0 && vcu >= rem_) convert_deferred(P, lds, 5); } } SEAM(9);
.LBB0_1609:
	s_abs_i32 s0, s62
	v_cvt_f32_u32_e32 v2, s0
	s_sub_i32 s5, 0, s0
	s_abs_i32 s4, s9
	s_ashr_i32 s3, s9, 31
	v_rcp_iflag_f32_e32 v2, v2
	s_mov_b32 s1, 0
	v_mul_f32_e32 v2, 0x4f7ffffe, v2
	v_cvt_u32_f32_e32 v2, v2
	s_nop 0
	v_readfirstlane_b32 s6, v2
	s_mul_i32 s5, s5, s6
	s_mul_hi_u32 s5, s6, s5
	s_add_i32 s6, s6, s5
	s_mul_hi_u32 s5, s4, s6
	s_mul_i32 s5, s5, s0
	s_sub_i32 s4, s4, s5
	s_sub_i32 s5, s4, s0
	s_cmp_ge_u32 s4, s0
	s_cselect_b32 s4, s5, s4
	s_sub_i32 s5, s4, s0
	s_cmp_ge_u32 s4, s0
	s_cselect_b32 s0, s5, s4
	s_xor_b32 s0, s0, s3
	s_sub_i32 s0, s0, s3
	s_cmp_eq_u32 s0, 0
	v_readlane_b32 s3, v254, 2
	s_cselect_b64 s[4:5], -1, 0
	s_cmp_lt_i32 s3, s0
	s_cselect_b64 s[6:7], -1, 0
	s_or_b64 s[4:5], s[4:5], s[6:7]
	s_and_b64 vcc, exec, s[4:5]
	s_cbranch_vccnz .LBB0_1619
	v_and_b32_e32 v2, 0x7c, v175
	v_lshlrev_b32_e32 v3, 5, v0
	s_movk_i32 s0, 0x400
	v_and_or_b32 v12, v3, s0, v2
	v_bfe_u32 v2, v0, 3, 3
	v_lshl_or_b32 v4, v1, 5, v2
	v_lshlrev_b32_e32 v2, 3, v0
	v_lshl_add_u32 v11, v182, 4, 0
	v_and_b32_e32 v2, 56, v2
	v_mul_u32_u24_e32 v16, 0x2020, v1
	v_mov_b32_e32 v3, 0
	v_lshl_add_u32 v27, v4, 2, 0
	v_mul_u32_u24_e32 v28, 0x404, v2
	v_lshlrev_b32_e32 v10, 6, v4
	s_add_i32 s10, 0, 0x22c38
	v_add_u32_e32 v16, v11, v16
	s_mov_b32 s3, 8
	v_and_b32_e32 v13, 0xfc, v175
	v_and_b32_e32 v14, 56, v173
	v_or_b32_e32 v4, 0x200, v10
	v_mov_b32_e32 v5, v3
	v_or_b32_e32 v6, 0x400, v10
	v_mov_b32_e32 v7, v3
	v_or_b32_e32 v8, 0x600, v10
	v_mov_b32_e32 v9, v3
	v_mov_b32_e32 v15, s10
	s_movk_i32 s11, 0x13eb
	s_movk_i32 s12, 0x800
	s_mov_b32 s13, 0x1104e000
	s_movk_i32 s14, -1004
	v_add_u32_e32 v17, 0x404, v16
	v_add_u32_e32 v18, 0x40c, v16
	v_add_u32_e32 v19, 0x808, v16
	v_add_u32_e32 v20, 0xc0c, v16
	v_add_u32_e32 v21, 0xc14, v16
	v_add_u32_e32 v22, 0x1414, v16
	v_add_u32_e32 v23, 0x141c, v16
	v_add_u32_e32 v24, 0x1818, v16
	v_add_u32_e32 v25, 0x1c1c, v16
	v_add_u32_e32 v26, 0x1c24, v16
	v_lshlrev_b32_e32 v2, 1, v2
	v_add_u32_e32 v27, v27, v28
	v_lshlrev_b32_e32 v10, 1, v10
	s_branch .LBB0_1612

; __device__ __forceinline__ unsigned g8_cvt_pk(float lo, float hi) { unsigned r; asm volatile("v_cvt_pk_bf16_f32 %0, %1, %2" : "=v"(r) : "v"(lo), "v"(hi)); return r; }
; __device__ __forceinline__ void bt_load(const float* __restrict__ src, int N, int perm, int it, int ntn, f32x4 (&v)[8]) {
;     const int wid = threadIdx.x >> 6, lane = threadIdx.x & 63;
;     const int per = 16 * ntn, z = it / per, r = it % per, kt = r / ntn, nt = r % ntn;
;     const int np = nt * 256 + lane * 4;
;     const int sc = perm ? (nt * 128 + (lane & 31) * 4 + (lane >> 5) * 1024) : np;
;     const float* p = src + (size_t)z * 1024 * N + (size_t)(kt * 64 + wid * 8) * N + sc;
; #pragma unroll
;     for (int i = 0; i < 8; ++i) v[i] = __builtin_nontemporal_load((const f32x4*)(p + (size_t)i * N));
; }
; __device__ __forceinline__ void convert_deferred(const Ptrs& P, unsigned char* lds, int quota) {
;     ...
;         __syncthreads();
;         if (tid == 0) *slot = (int)atomicAdd(q, 1u);
;         __syncthreads();
;         const int t = *slot;
;         if (t >= DEF_GU + DEF_DN) break;
;         const bool gu = t < DEF_GU;
;         const float* src = gu ? P.in[34] : P.in[36]; bf16* dst = (bf16*)(P.ws + (gu ? WS_WGU : WS_WDN));
;         const int N = gu ? 2048 : 1024, ntn = N / 256, it = gu ? 2 * NE * 16 * 8 - DEF_GU + t : 2 * NE * 16 * 4 - DEF_DN + (t - DEF_GU);
;         f32x4 cur[8];
;         bt_load(src, N, gu ? 1 : 0, it, ntn, cur);
; #pragma unroll
;         for (int i = 0; i < 8; ++i) { float* tp = tile + (wid * 8 + i) * 257 + lane * 4; tp[0] = cur[i][0]; tp[1] = cur[i][1]; tp[2] = cur[i][2]; tp[3] = cur[i][3]; }
;         __syncthreads();
;         const int per = 16 * ntn, z = it / per, r = it % per, kt = r / ntn, nt = r % ntn;
;         bf16* d = dst + (size_t)z * N * 1024 + (((size_t)nt * 16 + kt) << 14);
;         const int kc = lane & 7;
; #pragma unroll
;         for (int pss = 0; pss < 4; ++pss) {
;             const int nn = wid * 32 + pss * 8 + (lane >> 3); float f[8];
; #pragma unroll
;             for (int j = 0; j < 8; ++j) f[j] = tile[(kc * 8 + j) * 257 + nn];
;             u32x4 w; w.x = g8_cvt_pk(f[0], f[1]); w.y = g8_cvt_pk(f[2], f[3]); w.z = g8_cvt_pk(f[4], f[5]); w.w = g8_cvt_pk(f[6], f[7]);
;             *(u32x4*)(d + nn * 64 + kc * 8) = w;
;         }
.LBB0_1616:
	s_or_b64 exec, exec, s[4:5]
	s_waitcnt lgkmcnt(0)
	s_barrier
	ds_read_b32 v11, v15
	s_mov_b64 s[4:5], -1
	s_waitcnt lgkmcnt(0)
	v_cmp_lt_i32_e32 vcc, s11, v11
	v_readfirstlane_b32 s0, v11
	s_cbranch_vccnz .LBB0_1611
	s_cmpk_gt_i32 s0, 0xd47
	s_cselect_b64 vcc, -1, 0
	s_and_b64 s[4:5], vcc, exec
	s_cselect_b32 s4, s13, 0x104e000
	s_cselect_b32 s9, 0x400, s12
	s_cselect_b32 s15, s73, s69
	s_cselect_b32 s18, s72, s68
	s_cselect_b32 s5, s14, 0x12b8
	s_cselect_b32 s16, 20, 21
	s_cselect_b32 s19, 10, 11
	s_add_u32 s20, s78, s4
	s_addc_u32 s21, s79, 0
	s_lshr_b32 s6, s9, 4
	s_abs_i32 s4, s6
	v_cvt_f32_u32_e32 v11, s4
	s_sub_i32 s17, 0, s4
	s_add_i32 s5, s5, s0
	s_abs_i32 s7, s5
	v_rcp_iflag_f32_e32 v11, v11
	s_xor_b32 s0, s5, s6
	s_lshr_b32 s8, s9, 8
	s_ashr_i32 s0, s0, 31
	v_mul_f32_e32 v11, 0x4f7ffffe, v11
	v_cvt_u32_f32_e32 v11, v11
	s_nop 0
	v_readfirstlane_b32 s22, v11
	s_mul_i32 s17, s17, s22
	s_mul_hi_u32 s17, s22, s17
	s_add_i32 s22, s22, s17
	s_mul_hi_u32 s17, s7, s22
	s_mul_i32 s22, s17, s4
	s_sub_i32 s7, s7, s22
	s_add_i32 s22, s17, 1
	s_sub_i32 s23, s7, s4
	s_cmp_ge_u32 s7, s4
	s_cselect_b32 s17, s22, s17
	s_cselect_b32 s7, s23, s7
	s_add_i32 s22, s17, 1
	s_cmp_ge_u32 s7, s4
	s_cselect_b32 s4, s22, s17
	s_xor_b32 s4, s4, s0
	s_sub_i32 s4, s4, s0
	s_sext_i32_i8 s0, s8
	v_cvt_f32_i32_e32 v11, s0
	s_mul_i32 s6, s4, s6
	s_sub_i32 s5, s5, s6
	v_cvt_f32_i32_e32 v28, s5
	v_rcp_iflag_f32_e32 v29, v11
	s_xor_b32 s0, s5, s0
	s_ashr_i32 s0, s0, 30
	s_or_b32 s0, s0, 1
	v_mul_f32_e32 v29, v28, v29
	v_trunc_f32_e32 v29, v29
	v_fma_f32 v28, -v29, v11, v28
	v_cvt_i32_f32_e32 v29, v29
	v_cmp_ge_f32_e64 s[6:7], |v28|, |v11|
	s_and_b64 s[6:7], s[6:7], exec
	s_cselect_b32 s0, s0, 0
	v_readfirstlane_b32 s6, v29
	s_add_i32 s6, s6, s0
	s_mul_i32 s7, s6, s8
	s_sub_i32 s8, s5, s7
	s_sext_i32_i8 s5, s8
	v_lshl_add_u32 v11, s5, 7, v12
	v_lshl_or_b32 v28, s5, 8, v13
	s_ashr_i32 s5, s4, 31
	s_sext_i32_i8 s0, s6
	s_lshl_b64 s[16:17], s[4:5], s16
	v_lshl_or_b32 v30, s0, 6, v14
	s_lshl_b64 s[16:17], s[16:17], 2
	v_ashrrev_i32_e32 v31, 31, v30
	s_add_u32 s16, s18, s16
	v_cndmask_b32_e32 v28, v11, v28, vcc
	s_addc_u32 s17, s15, s17
	v_lshlrev_b64 v[30:31], s19, v[30:31]
	v_lshl_add_u64 v[30:31], v[30:31], 2, s[16:17]
	v_ashrrev_i32_e32 v29, 31, v28
	v_lshl_add_u64 v[52:53], v[28:29], 2, v[30:31]
	s_lshl_b64 s[16:17], 12, s19
	s_lshl_b32 s0, s9, 2
	v_lshl_add_u64 v[40:41], v[52:53], 0, s[16:17]
	s_lshl_b64 s[16:17], 24, s19
	v_lshl_add_u64 v[36:37], v[52:53], 0, s[0:1]
	v_lshl_add_u64 v[44:45], v[52:53], 0, s[16:17]
	s_lshl_b64 s[16:17], 28, s19
	v_lshl_add_u64 v[54:55], v[36:37], 0, s[0:1]
	v_lshl_add_u64 v[48:49], v[52:53], 0, s[16:17]
	s_lshl_b32 s0, s9, 3
	s_lshl_b64 s[16:17], 20, s19
	global_load_dwordx4 v[28:31], v[52:53], off nt
	global_load_dwordx4 v[32:35], v[36:37], off nt
	s_nop 0
	global_load_dwordx4 v[36:39], v[54:55], off nt
	s_nop 0
	global_load_dwordx4 v[40:43], v[40:41], off nt
	v_lshl_add_u64 v[54:55], v[54:55], 0, s[0:1]
	v_lshl_add_u64 v[56:57], v[52:53], 0, s[16:17]
	global_load_dwordx4 v[44:47], v[44:45], off nt
	s_nop 0
	global_load_dwordx4 v[48:51], v[48:49], off nt
	s_nop 0
	global_load_dwordx4 v[52:55], v[54:55], off nt
	s_nop 0
	global_load_dwordx4 v[56:59], v[56:57], off nt
	s_lshl_b64 s[4:5], s[4:5], s19
	s_lshl_b64 s[4:5], s[4:5], 11
	s_add_u32 s0, s20, s4
	s_addc_u32 s9, s21, s5
	s_bfe_i64 s[4:5], s[8:9], 0x80000
	s_bfe_i64 s[6:7], s[6:7], 0x80000
	s_lshl_b64 s[4:5], s[4:5], 19
	s_add_u32 s0, s0, s4
	s_addc_u32 s8, s9, s5
	s_lshl_b64 s[4:5], s[6:7], 15
	s_add_u32 s4, s0, s4
	s_addc_u32 s5, s8, s5
	v_mov_b32_e32 v11, v3
	s_add_i32 s3, s3, -1
	s_cmp_eq_u32 s3, 0
	s_waitcnt vmcnt(7)
	ds_write_b128 v16, v[28:31]
	s_waitcnt vmcnt(6)
	ds_write2_b32 v17, v32, v33 offset1:1
	ds_write2_b32 v18, v34, v35 offset1:1
	s_waitcnt vmcnt(3)
	ds_write2_b64 v24, v[44:45], v[46:47] offset1:1
	s_waitcnt vmcnt(2)
	ds_write2_b32 v25, v48, v49 offset1:1
	ds_write2_b32 v26, v50, v51 offset1:1
	ds_write2_b64 v19, v[36:37], v[38:39] offset1:1
	ds_write2_b32 v20, v40, v41 offset1:1
	ds_write2_b32 v21, v42, v43 offset1:1
	s_waitcnt vmcnt(1)
	ds_write_b128 v16, v[52:55] offset:4112
	s_waitcnt vmcnt(0)
	ds_write2_b32 v22, v56, v57 offset1:1
	ds_write2_b32 v23, v58, v59 offset1:1
	s_waitcnt lgkmcnt(0)
	s_barrier
	ds_read_b32 v28, v27 offset:1028
	ds_read_b32 v29, v27 offset:3084
	ds_read_b32 v30, v27 offset:5140
	ds_read_b32 v31, v27 offset:7196
	ds_read_b32 v32, v27 offset:6168
	ds_read_b32 v33, v27 offset:4112
	ds_read_b32 v34, v27 offset:2056
	ds_read_b32 v35, v27
	s_waitcnt lgkmcnt(0)
	v_cvt_pk_bf16_f32 v28, v35, v28
	v_cvt_pk_bf16_f32 v29, v34, v29
	v_cvt_pk_bf16_f32 v30, v33, v30
	v_cvt_pk_bf16_f32 v31, v32, v31
	ds_read_b32 v36, v27 offset:1060
	ds_read_b32 v37, v27 offset:3116
	ds_read_b32 v38, v27 offset:5172
	ds_read_b32 v39, v27 offset:7228
	ds_read_b32 v40, v27 offset:6200
	ds_read_b32 v41, v27 offset:4144
	ds_read_b32 v42, v27 offset:2088
	ds_read_b32 v43, v27 offset:32
	v_lshl_add_u64 v[32:33], s[4:5], 0, v[2:3]
	v_lshl_add_u64 v[34:35], v[32:33], 0, v[10:11]
	global_store_dwordx4 v[34:35], v[28:31], off
	v_lshl_add_u64 v[34:35], v[4:5], 1, v[32:33]
	s_cselect_b64 s[4:5], -1, 0
	s_waitcnt lgkmcnt(0)
	v_cvt_pk_bf16_f32 v28, v43, v36
	v_cvt_pk_bf16_f32 v29, v42, v37
	v_cvt_pk_bf16_f32 v30, v41, v38
	v_cvt_pk_bf16_f32 v31, v40, v39
	ds_read_b32 v11, v27 offset:1092
	ds_read_b32 v36, v27 offset:3148
	ds_read_b32 v37, v27 offset:6232
	ds_read_b32 v38, v27 offset:4176
	ds_read_b32 v39, v27 offset:2120
	ds_read_b32 v40, v27 offset:64
	ds_read_b32 v41, v27 offset:5204
	ds_read_b32 v42, v27 offset:7260
	global_store_dwordx4 v[34:35], v[28:31], off
	v_lshl_add_u64 v[34:35], v[6:7], 1, v[32:33]
	v_lshl_add_u64 v[32:33], v[8:9], 1, v[32:33]
	s_waitcnt lgkmcnt(2)
	v_cvt_pk_bf16_f32 v28, v40, v11
	v_cvt_pk_bf16_f32 v29, v39, v36
	s_waitcnt lgkmcnt(1)
	v_cvt_pk_bf16_f32 v30, v38, v41
	s_waitcnt lgkmcnt(0)
	v_cvt_pk_bf16_f32 v31, v37, v42
	ds_read_b32 v11, v27 offset:1124
	ds_read_b32 v36, v27 offset:3180
	ds_read_b32 v37, v27 offset:6264
	ds_read_b32 v38, v27 offset:4208
	ds_read_b32 v39, v27 offset:2152
	ds_read_b32 v40, v27 offset:96
	ds_read_b32 v41, v27 offset:5236
	ds_read_b32 v42, v27 offset:7292
	global_store_dwordx4 v[34:35], v[28:31], off
	s_waitcnt lgkmcnt(2)
	s_nop 0
	v_cvt_pk_bf16_f32 v28, v40, v11
	v_cvt_pk_bf16_f32 v29, v39, v36
	s_waitcnt lgkmcnt(1)
	v_cvt_pk_bf16_f32 v30, v38, v41
	s_waitcnt lgkmcnt(0)
	v_cvt_pk_bf16_f32 v31, v37, v42
	global_store_dwordx4 v[32:33], v[28:31], off
	s_branch .LBB0_1611

; #define SEAM(k) do { if (IN(k) && IN((k) + 1)) xcd_barrier(bar); \
;         if (PROBE_MASK) { const unsigned long long t_ = __builtin_amdgcn_s_memrealtime(); if ((PROBE_MASK >> (k)) & 1u) pr_acc += t_ - pr_t0; pr_t0 = t_; } } while (0)
; __device__ __forceinline__ void convert_deferred(const Ptrs& P, unsigned char* lds, int quota) {
;     const int tid = threadIdx.x, wid = tid >> 6, lane = tid & 63;
;     float* tile = (float*)lds;
;     volatile __attribute__((address_space(3))) int* slot = (volatile __attribute__((address_space(3))) int*)((__attribute__((address_space(3))) unsigned char*)lds + 131072 + 320 + 11000);
;     unsigned* q = (unsigned*)(P.ws + WS_CTL) + CW_DEFQ;
;     for (int n = 0; n < quota; ++n) {
;         __syncthreads();
;         if (tid == 0) *slot = (int)atomicAdd(q, 1u);
;         __syncthreads();
;         const int t = *slot;
;         if (t >= DEF_GU + DEF_DN) break;
;         const bool gu = t < DEF_GU;
;         const float* src = gu ? P.in[34] : P.in[36]; bf16* dst = (bf16*)(P.ws + (gu ? WS_WGU : WS_WDN));
;         const int N = gu ? 2048 : 1024, ntn = N / 256, it = gu ? 2 * NE * 16 * 8 - DEF_GU + t : 2 * NE * 16 * 4 - DEF_DN + (t - DEF_GU);
; __global__ void __launch_bounds__(NT, 2) mega(Args args) {
;     ...
;         if (IDLE_LAST(68 * 12)) convert_deferred(P, lds, 4); } SEAM(11);
.LBB0_1851:
	s_abs_i32 s0, s62
	v_cvt_f32_u32_e32 v2, s0
	s_sub_i32 s3, 0, s0
	v_readlane_b32 s56, v254, 40
	s_mov_b32 s1, 0
	v_rcp_iflag_f32_e32 v2, v2
	v_readlane_b32 s57, v254, 41
	v_mul_f32_e32 v2, 0x4f7ffffe, v2
	v_cvt_u32_f32_e32 v2, v2
	s_nop 0
	v_readfirstlane_b32 s4, v2
	s_mul_i32 s3, s3, s4
	s_mul_hi_u32 s3, s4, s3
	s_add_i32 s4, s4, s3
	s_mul_hi_u32 s3, s4, 0x330
	s_mul_i32 s3, s3, s0
	s_sub_i32 s3, 0x330, s3
	s_sub_i32 s4, s3, s0
	s_cmp_ge_u32 s3, s0
	s_cselect_b32 s3, s4, s3
	s_sub_i32 s4, s3, s0
	s_cmp_ge_u32 s3, s0
	s_cselect_b32 s0, s4, s3
	s_cmp_eq_u32 s0, 0
	s_cselect_b64 s[4:5], -1, 0
	s_cmp_lt_i32 s2, s0
	s_cselect_b64 s[6:7], -1, 0
	s_or_b64 s[4:5], s[4:5], s[6:7]
	s_and_b64 vcc, exec, s[4:5]
	s_cbranch_vccnz .LBB0_1861
	v_and_b32_e32 v2, 0x7c, v218
	v_lshlrev_b32_e32 v3, 5, v0
	s_movk_i32 s0, 0x400
	v_and_or_b32 v12, v3, s0, v2
	v_bfe_u32 v2, v0, 3, 3
	v_lshl_or_b32 v4, v1, 5, v2
	v_lshlrev_b32_e32 v2, 3, v0
	v_lshl_add_u32 v11, v182, 4, 0
	v_and_b32_e32 v2, 56, v2
	v_mul_u32_u24_e32 v16, 0x2020, v1
	v_mov_b32_e32 v3, 0
	s_waitcnt vmcnt(0)
	v_lshl_add_u32 v27, v4, 2, 0
	v_mul_u32_u24_e32 v28, 0x404, v2
	v_lshlrev_b32_e32 v10, 6, v4
	s_add_i32 s10, 0, 0x22c38
	v_add_u32_e32 v16, v11, v16
	v_and_b32_e32 v13, 0xfc, v218
	v_and_b32_e32 v14, 56, v179
	s_mov_b32 s3, 10
	v_or_b32_e32 v4, 0x200, v10
	v_mov_b32_e32 v5, v3
	v_or_b32_e32 v6, 0x400, v10
	v_mov_b32_e32 v7, v3
	v_or_b32_e32 v8, 0x600, v10
	v_mov_b32_e32 v9, v3
	v_mov_b32_e32 v15, s10
	s_movk_i32 s11, 0x13eb
	s_movk_i32 s12, 0x800
	s_mov_b32 s13, 0x1104e000
	s_movk_i32 s14, -1004
	v_add_u32_e32 v17, 0x404, v16
	v_add_u32_e32 v18, 0x40c, v16
	v_add_u32_e32 v19, 0x808, v16
	v_add_u32_e32 v20, 0xc0c, v16
	v_add_u32_e32 v21, 0xc14, v16
	v_add_u32_e32 v22, 0x1414, v16
	v_add_u32_e32 v23, 0x141c, v16
	v_add_u32_e32 v24, 0x1818, v16
	v_add_u32_e32 v25, 0x1c1c, v16
	v_add_u32_e32 v26, 0x1c24, v16
	v_lshlrev_b32_e32 v2, 1, v2
	v_add_u32_e32 v27, v27, v28
	v_lshlrev_b32_e32 v10, 1, v10
	s_branch .LBB0_1854

; __device__ __forceinline__ unsigned g8_cvt_pk(float lo, float hi) { unsigned r; asm volatile("v_cvt_pk_bf16_f32 %0, %1, %2" : "=v"(r) : "v"(lo), "v"(hi)); return r; }
; __device__ __forceinline__ void bt_load(const float* __restrict__ src, int N, int perm, int it, int ntn, f32x4 (&v)[8]) {
;     const int wid = threadIdx.x >> 6, lane = threadIdx.x & 63;
;     const int per = 16 * ntn, z = it / per, r = it % per, kt = r / ntn, nt = r % ntn;
;     const int np = nt * 256 + lane * 4;
;     const int sc = perm ? (nt * 128 + (lane & 31) * 4 + (lane >> 5) * 1024) : np;
;     const float* p = src + (size_t)z * 1024 * N + (size_t)(kt * 64 + wid * 8) * N + sc;
; #pragma unroll
;     for (int i = 0; i < 8; ++i) v[i] = __builtin_nontemporal_load((const f32x4*)(p + (size_t)i * N));
; }
; __device__ __forceinline__ void convert_deferred(const Ptrs& P, unsigned char* lds, int quota) {
;     ...
;         __syncthreads();
;         if (tid == 0) *slot = (int)atomicAdd(q, 1u);
;         __syncthreads();
;         const int t = *slot;
;         if (t >= DEF_GU + DEF_DN) break;
;         const bool gu = t < DEF_GU;
;         const float* src = gu ? P.in[34] : P.in[36]; bf16* dst = (bf16*)(P.ws + (gu ? WS_WGU : WS_WDN));
;         const int N = gu ? 2048 : 1024, ntn = N / 256, it = gu ? 2 * NE * 16 * 8 - DEF_GU + t : 2 * NE * 16 * 4 - DEF_DN + (t - DEF_GU);
;         f32x4 cur[8];
;         bt_load(src, N, gu ? 1 : 0, it, ntn, cur);
; #pragma unroll
;         for (int i = 0; i < 8; ++i) { float* tp = tile + (wid * 8 + i) * 257 + lane * 4; tp[0] = cur[i][0]; tp[1] = cur[i][1]; tp[2] = cur[i][2]; tp[3] = cur[i][3]; }
;         __syncthreads();
;         const int per = 16 * ntn, z = it / per, r = it % per, kt = r / ntn, nt = r % ntn;
;         bf16* d = dst + (size_t)z * N * 1024 + (((size_t)nt * 16 + kt) << 14);
;         const int kc = lane & 7;
; #pragma unroll
;         for (int pss = 0; pss < 4; ++pss) {
;             const int nn = wid * 32 + pss * 8 + (lane >> 3); float f[8];
; #pragma unroll
;             for (int j = 0; j < 8; ++j) f[j] = tile[(kc * 8 + j) * 257 + nn];
;             u32x4 w; w.x = g8_cvt_pk(f[0], f[1]); w.y = g8_cvt_pk(f[2], f[3]); w.z = g8_cvt_pk(f[4], f[5]); w.w = g8_cvt_pk(f[6], f[7]);
;             *(u32x4*)(d + nn * 64 + kc * 8) = w;
;         }
.LBB0_1858:
	s_or_b64 exec, exec, s[4:5]
	s_waitcnt lgkmcnt(0)
	s_barrier
	ds_read_b32 v11, v15
	s_mov_b64 s[4:5], -1
	s_waitcnt lgkmcnt(0)
	v_cmp_lt_i32_e32 vcc, s11, v11
	v_readfirstlane_b32 s0, v11
	s_cbranch_vccnz .LBB0_1853
	s_cmpk_gt_i32 s0, 0xd47
	s_cselect_b64 vcc, -1, 0
	s_and_b64 s[4:5], vcc, exec
	s_cselect_b32 s4, s13, 0x104e000
	s_cselect_b32 s9, 0x400, s12
	s_cselect_b32 s15, s73, s69
	s_cselect_b32 s20, s72, s68
	s_cselect_b32 s5, s14, 0x12b8
	s_cselect_b32 s16, 20, 21
	s_cselect_b32 s21, 10, 11
	s_add_u32 s22, s78, s4
	s_addc_u32 s23, s79, 0
	s_lshr_b32 s6, s9, 4
	s_abs_i32 s4, s6
	v_cvt_f32_u32_e32 v11, s4
	s_sub_i32 s17, 0, s4
	s_add_i32 s5, s5, s0
	s_abs_i32 s7, s5
	v_rcp_iflag_f32_e32 v11, v11
	s_xor_b32 s0, s5, s6
	s_lshr_b32 s8, s9, 8
	s_ashr_i32 s0, s0, 31
	v_mul_f32_e32 v11, 0x4f7ffffe, v11
	v_cvt_u32_f32_e32 v11, v11
	s_nop 0
	v_readfirstlane_b32 s24, v11
	s_mul_i32 s17, s17, s24
	s_mul_hi_u32 s17, s24, s17
	s_add_i32 s24, s24, s17
	s_mul_hi_u32 s17, s7, s24
	s_mul_i32 s24, s17, s4
	s_sub_i32 s7, s7, s24
	s_add_i32 s24, s17, 1
	s_sub_i32 s25, s7, s4
	s_cmp_ge_u32 s7, s4
	s_cselect_b32 s17, s24, s17
	s_cselect_b32 s7, s25, s7
	s_add_i32 s24, s17, 1
	s_cmp_ge_u32 s7, s4
	s_cselect_b32 s4, s24, s17
	s_xor_b32 s4, s4, s0
	s_sub_i32 s4, s4, s0
	s_sext_i32_i8 s0, s8
	v_cvt_f32_i32_e32 v11, s0
	s_mul_i32 s6, s4, s6
	s_sub_i32 s5, s5, s6
	v_cvt_f32_i32_e32 v28, s5
	v_rcp_iflag_f32_e32 v29, v11
	s_xor_b32 s0, s5, s0
	s_ashr_i32 s0, s0, 30
	s_or_b32 s0, s0, 1
	v_mul_f32_e32 v29, v28, v29
	v_trunc_f32_e32 v29, v29
	v_fma_f32 v28, -v29, v11, v28
	v_cvt_i32_f32_e32 v29, v29
	v_cmp_ge_f32_e64 s[6:7], |v28|, |v11|
	s_and_b64 s[6:7], s[6:7], exec
	s_cselect_b32 s0, s0, 0
	v_readfirstlane_b32 s6, v29
	s_add_i32 s6, s6, s0
	s_mul_i32 s7, s6, s8
	s_sub_i32 s8, s5, s7
	s_sext_i32_i8 s5, s8
	v_lshl_add_u32 v11, s5, 7, v12
	v_lshl_or_b32 v28, s5, 8, v13
	s_ashr_i32 s5, s4, 31
	s_sext_i32_i8 s0, s6
	s_lshl_b64 s[16:17], s[4:5], s16
	v_lshl_or_b32 v30, s0, 6, v14
	s_lshl_b64 s[16:17], s[16:17], 2
	v_ashrrev_i32_e32 v31, 31, v30
	s_add_u32 s16, s20, s16
	v_cndmask_b32_e32 v28, v11, v28, vcc
	s_addc_u32 s17, s15, s17
	v_lshlrev_b64 v[30:31], s21, v[30:31]
	v_lshl_add_u64 v[30:31], v[30:31], 2, s[16:17]
	v_ashrrev_i32_e32 v29, 31, v28
	v_lshl_add_u64 v[52:53], v[28:29], 2, v[30:31]
	s_lshl_b64 s[16:17], 12, s21
	s_lshl_b32 s0, s9, 2
	v_lshl_add_u64 v[40:41], v[52:53], 0, s[16:17]
	s_lshl_b64 s[16:17], 24, s21
	v_lshl_add_u64 v[36:37], v[52:53], 0, s[0:1]
	v_lshl_add_u64 v[44:45], v[52:53], 0, s[16:17]
	s_lshl_b64 s[16:17], 28, s21
	v_lshl_add_u64 v[54:55], v[36:37], 0, s[0:1]
	v_lshl_add_u64 v[48:49], v[52:53], 0, s[16:17]
	s_lshl_b32 s0, s9, 3
	s_lshl_b64 s[16:17], 20, s21
	global_load_dwordx4 v[28:31], v[52:53], off nt
	global_load_dwordx4 v[32:35], v[36:37], off nt
	s_nop 0
	global_load_dwordx4 v[36:39], v[54:55], off nt
	s_nop 0
	global_load_dwordx4 v[40:43], v[40:41], off nt
	v_lshl_add_u64 v[54:55], v[54:55], 0, s[0:1]
	v_lshl_add_u64 v[56:57], v[52:53], 0, s[16:17]
	global_load_dwordx4 v[44:47], v[44:45], off nt
	s_nop 0
	global_load_dwordx4 v[48:51], v[48:49], off nt
	s_nop 0
	global_load_dwordx4 v[52:55], v[54:55], off nt
	s_nop 0
	global_load_dwordx4 v[56:59], v[56:57], off nt
	s_lshl_b64 s[4:5], s[4:5], s21
	s_lshl_b64 s[4:5], s[4:5], 11
	s_add_u32 s0, s22, s4
	s_addc_u32 s9, s23, s5
	s_bfe_i64 s[4:5], s[8:9], 0x80000
	s_bfe_i64 s[6:7], s[6:7], 0x80000
	s_lshl_b64 s[4:5], s[4:5], 19
	s_add_u32 s0, s0, s4
	s_addc_u32 s8, s9, s5
	s_lshl_b64 s[4:5], s[6:7], 15
	s_add_u32 s4, s0, s4
	s_addc_u32 s5, s8, s5
	v_mov_b32_e32 v11, v3
	s_add_i32 s3, s3, -1
	s_cmp_eq_u32 s3, 0
	s_waitcnt vmcnt(7)
	ds_write_b128 v16, v[28:31]
	s_waitcnt vmcnt(6)
	ds_write2_b32 v17, v32, v33 offset1:1
	ds_write2_b32 v18, v34, v35 offset1:1
	s_waitcnt vmcnt(3)
	ds_write2_b64 v24, v[44:45], v[46:47] offset1:1
	s_waitcnt vmcnt(2)
	ds_write2_b32 v25, v48, v49 offset1:1
	ds_write2_b32 v26, v50, v51 offset1:1
	ds_write2_b64 v19, v[36:37], v[38:39] offset1:1
	ds_write2_b32 v20, v40, v41 offset1:1
	ds_write2_b32 v21, v42, v43 offset1:1
	s_waitcnt vmcnt(1)
	ds_write_b128 v16, v[52:55] offset:4112
	s_waitcnt vmcnt(0)
	ds_write2_b32 v22, v56, v57 offset1:1
	ds_write2_b32 v23, v58, v59 offset1:1
	s_waitcnt lgkmcnt(0)
	s_barrier
	ds_read_b32 v28, v27 offset:1028
	ds_read_b32 v29, v27 offset:3084
	ds_read_b32 v30, v27 offset:5140
	ds_read_b32 v31, v27 offset:7196
	ds_read_b32 v32, v27 offset:6168
	ds_read_b32 v33, v27 offset:4112
	ds_read_b32 v34, v27 offset:2056
	ds_read_b32 v35, v27
	s_waitcnt lgkmcnt(0)
	v_cvt_pk_bf16_f32 v28, v35, v28
	v_cvt_pk_bf16_f32 v29, v34, v29
	v_cvt_pk_bf16_f32 v30, v33, v30
	v_cvt_pk_bf16_f32 v31, v32, v31
	ds_read_b32 v36, v27 offset:1060
	ds_read_b32 v37, v27 offset:3116
	ds_read_b32 v38, v27 offset:5172
	ds_read_b32 v39, v27 offset:7228
	ds_read_b32 v40, v27 offset:6200
	ds_read_b32 v41, v27 offset:4144
	ds_read_b32 v42, v27 offset:2088
	ds_read_b32 v43, v27 offset:32
	v_lshl_add_u64 v[32:33], s[4:5], 0, v[2:3]
	v_lshl_add_u64 v[34:35], v[32:33], 0, v[10:11]
	global_store_dwordx4 v[34:35], v[28:31], off
	v_lshl_add_u64 v[34:35], v[4:5], 1, v[32:33]
	s_cselect_b64 s[4:5], -1, 0
	s_waitcnt lgkmcnt(0)
	v_cvt_pk_bf16_f32 v28, v43, v36
	v_cvt_pk_bf16_f32 v29, v42, v37
	v_cvt_pk_bf16_f32 v30, v41, v38
	v_cvt_pk_bf16_f32 v31, v40, v39
	ds_read_b32 v11, v27 offset:1092
	ds_read_b32 v36, v27 offset:3148
	ds_read_b32 v37, v27 offset:6232
	ds_read_b32 v38, v27 offset:4176
	ds_read_b32 v39, v27 offset:2120
	ds_read_b32 v40, v27 offset:64
	ds_read_b32 v41, v27 offset:5204
	ds_read_b32 v42, v27 offset:7260
	global_store_dwordx4 v[34:35], v[28:31], off
	v_lshl_add_u64 v[34:35], v[6:7], 1, v[32:33]
	v_lshl_add_u64 v[32:33], v[8:9], 1, v[32:33]
	s_waitcnt lgkmcnt(2)
	v_cvt_pk_bf16_f32 v28, v40, v11
	v_cvt_pk_bf16_f32 v29, v39, v36
	s_waitcnt lgkmcnt(1)
	v_cvt_pk_bf16_f32 v30, v38, v41
	s_waitcnt lgkmcnt(0)
	v_cvt_pk_bf16_f32 v31, v37, v42
	ds_read_b32 v11, v27 offset:1124
	ds_read_b32 v36, v27 offset:3180
	ds_read_b32 v37, v27 offset:6264
	ds_read_b32 v38, v27 offset:4208
	ds_read_b32 v39, v27 offset:2152
	ds_read_b32 v40, v27 offset:96
	ds_read_b32 v41, v27 offset:5236
	ds_read_b32 v42, v27 offset:7292
	global_store_dwordx4 v[34:35], v[28:31], off
	s_waitcnt lgkmcnt(2)
	s_nop 0
	v_cvt_pk_bf16_f32 v28, v40, v11
	v_cvt_pk_bf16_f32 v29, v39, v36
	s_waitcnt lgkmcnt(1)
	v_cvt_pk_bf16_f32 v30, v38, v41
	s_waitcnt lgkmcnt(0)
	v_cvt_pk_bf16_f32 v31, v37, v42
	global_store_dwordx4 v[32:33], v[28:31], off
	s_branch .LBB0_1853

; #define SEAM(k) do { if (IN(k) && IN((k) + 1)) xcd_barrier(bar); \
;         if (PROBE_MASK) { const unsigned long long t_ = __builtin_amdgcn_s_memrealtime(); if ((PROBE_MASK >> (k)) & 1u) pr_acc += t_ - pr_t0; pr_t0 = t_; } } while (0)
; __device__ __forceinline__ void convert_deferred(const Ptrs& P, unsigned char* lds, int quota) {
;     const int tid = threadIdx.x, wid = tid >> 6, lane = tid & 63;
;     float* tile = (float*)lds;
;     volatile __attribute__((address_space(3))) int* slot = (volatile __attribute__((address_space(3))) int*)((__attribute__((address_space(3))) unsigned char*)lds + 131072 + 320 + 11000);
;     unsigned* q = (unsigned*)(P.ws + WS_CTL) + CW_DEFQ;
;     for (int n = 0; n < quota; ++n) {
;         __syncthreads();
;         if (tid == 0) *slot = (int)atomicAdd(q, 1u);
;         __syncthreads();
;         const int t = *slot;
;         if (t >= DEF_GU + DEF_DN) break;
;         const bool gu = t < DEF_GU;
;         const float* src = gu ? P.in[34] : P.in[36]; bf16* dst = (bf16*)(P.ws + (gu ? WS_WGU : WS_WDN));
;         const int N = gu ? 2048 : 1024, ntn = N / 256, it = gu ? 2 * NE * 16 * 8 - DEF_GU + t : 2 * NE * 16 * 4 - DEF_DN + (t - DEF_GU);
; __global__ void __launch_bounds__(NT, 2) mega(Args args) {
;     ...
;     if (IN(15)) { ph_norm2_router(P, lds, 1, 1); convert_deferred(P, lds, 1 << 20); } SEAM(15);
.LBB0_2278:
	v_and_b32_e32 v2, 0x7c, v179
	v_lshlrev_b32_e32 v3, 5, v0
	s_movk_i32 s0, 0x400
	v_and_or_b32 v12, v3, s0, v2
	v_lshrrev_b32_e32 v2, 3, v0
	v_and_b32_e32 v14, 56, v2
	v_lshrrev_b32_e32 v2, 3, v182
	v_lshl_or_b32 v4, v1, 5, v2
	v_lshl_add_u32 v5, v182, 4, 0
	v_and_b32_e32 v2, 56, v188
	v_lshl_add_u32 v7, v4, 2, 0
	v_mul_u32_u24_e32 v11, 0x2020, v1
	v_lshlrev_b32_e32 v4, 6, v4
	v_mul_u32_u24_e32 v9, 0x404, v2
	v_or_b32_e32 v6, 0x200, v4
	v_or_b32_e32 v8, 0x400, v4
	v_or_b32_e32 v10, 0x600, v4
	s_add_i32 s10, 0, 0x22c38
	v_add_u32_e32 v16, v5, v11
	v_and_b32_e32 v13, 0xfc, v179
	s_mov_b32 s1, 0
	v_mov_b32_e32 v3, 0
	s_mov_b32 s3, 0x100000
	v_mov_b32_e32 v15, s10
	s_movk_i32 s11, 0x13eb
	s_movk_i32 s12, 0x800
	s_mov_b32 s13, 0x1104e000
	s_movk_i32 s14, -1004
	v_add_u32_e32 v17, 0x404, v16
	v_add_u32_e32 v18, 0x40c, v16
	v_add_u32_e32 v19, 0x808, v16
	v_add_u32_e32 v20, 0xc0c, v16
	v_add_u32_e32 v21, 0xc14, v16
	v_add_u32_e32 v22, 0x1414, v16
	v_add_u32_e32 v23, 0x141c, v16
	v_add_u32_e32 v24, 0x1818, v16
	v_add_u32_e32 v25, 0x1c1c, v16
	v_add_u32_e32 v26, 0x1c24, v16
	v_lshlrev_b32_e32 v2, 1, v2
	v_add_u32_e32 v27, v7, v9
	v_lshlrev_b32_e32 v4, 1, v4
	v_lshlrev_b32_e32 v6, 1, v6
	v_lshlrev_b32_e32 v8, 1, v8
	v_lshlrev_b32_e32 v10, 1, v10
	s_branch .LBB0_2280

; __device__ __forceinline__ unsigned g8_cvt_pk(float lo, float hi) { unsigned r; asm volatile("v_cvt_pk_bf16_f32 %0, %1, %2" : "=v"(r) : "v"(lo), "v"(hi)); return r; }
; __device__ __forceinline__ void bt_load(const float* __restrict__ src, int N, int perm, int it, int ntn, f32x4 (&v)[8]) {
;     const int wid = threadIdx.x >> 6, lane = threadIdx.x & 63;
;     const int per = 16 * ntn, z = it / per, r = it % per, kt = r / ntn, nt = r % ntn;
;     const int np = nt * 256 + lane * 4;
;     const int sc = perm ? (nt * 128 + (lane & 31) * 4 + (lane >> 5) * 1024) : np;
;     const float* p = src + (size_t)z * 1024 * N + (size_t)(kt * 64 + wid * 8) * N + sc;
; #pragma unroll
;     for (int i = 0; i < 8; ++i) v[i] = __builtin_nontemporal_load((const f32x4*)(p + (size_t)i * N));
; }
; __device__ __forceinline__ void convert_deferred(const Ptrs& P, unsigned char* lds, int quota) {
;     ...
;         __syncthreads();
;         if (tid == 0) *slot = (int)atomicAdd(q, 1u);
;         __syncthreads();
;         const int t = *slot;
;         if (t >= DEF_GU + DEF_DN) break;
;         const bool gu = t < DEF_GU;
;         const float* src = gu ? P.in[34] : P.in[36]; bf16* dst = (bf16*)(P.ws + (gu ? WS_WGU : WS_WDN));
;         const int N = gu ? 2048 : 1024, ntn = N / 256, it = gu ? 2 * NE * 16 * 8 - DEF_GU + t : 2 * NE * 16 * 4 - DEF_DN + (t - DEF_GU);
;         f32x4 cur[8];
;         bt_load(src, N, gu ? 1 : 0, it, ntn, cur);
; #pragma unroll
;         for (int i = 0; i < 8; ++i) { float* tp = tile + (wid * 8 + i) * 257 + lane * 4; tp[0] = cur[i][0]; tp[1] = cur[i][1]; tp[2] = cur[i][2]; tp[3] = cur[i][3]; }
;         __syncthreads();
;         const int per = 16 * ntn, z = it / per, r = it % per, kt = r / ntn, nt = r % ntn;
;         bf16* d = dst + (size_t)z * N * 1024 + (((size_t)nt * 16 + kt) << 14);
;         const int kc = lane & 7;
; #pragma unroll
;         for (int pss = 0; pss < 4; ++pss) {
;             const int nn = wid * 32 + pss * 8 + (lane >> 3); float f[8];
; #pragma unroll
;             for (int j = 0; j < 8; ++j) f[j] = tile[(kc * 8 + j) * 257 + nn];
;             u32x4 w; w.x = g8_cvt_pk(f[0], f[1]); w.y = g8_cvt_pk(f[2], f[3]); w.z = g8_cvt_pk(f[4], f[5]); w.w = g8_cvt_pk(f[6], f[7]);
;             *(u32x4*)(d + nn * 64 + kc * 8) = w;
;         }
.LBB0_2284:
	s_or_b64 exec, exec, s[4:5]
	s_waitcnt lgkmcnt(0)
	s_barrier
	ds_read_b32 v5, v15
	s_mov_b64 s[4:5], -1
	s_waitcnt lgkmcnt(0)
	v_cmp_lt_i32_e32 vcc, s11, v5
	v_readfirstlane_b32 s0, v5
	s_cbranch_vccnz .LBB0_2279
	s_cmpk_gt_i32 s0, 0xd47
	s_cselect_b64 vcc, -1, 0
	s_and_b64 s[4:5], vcc, exec
	s_cselect_b32 s4, s13, 0x104e000
	s_cselect_b32 s9, 0x400, s12
	s_cselect_b32 s15, s73, s69
	s_cselect_b32 s18, s72, s68
	s_cselect_b32 s5, s14, 0x12b8
	s_cselect_b32 s16, 20, 21
	s_cselect_b32 s19, 10, 11
	s_add_u32 s22, s78, s4
	s_addc_u32 s23, s79, 0
	s_lshr_b32 s6, s9, 4
	s_abs_i32 s4, s6
	v_cvt_f32_u32_e32 v5, s4
	s_sub_i32 s17, 0, s4
	s_add_i32 s5, s5, s0
	s_abs_i32 s7, s5
	v_rcp_iflag_f32_e32 v5, v5
	s_xor_b32 s0, s5, s6
	s_lshr_b32 s8, s9, 8
	s_ashr_i32 s0, s0, 31
	v_mul_f32_e32 v5, 0x4f7ffffe, v5
	v_cvt_u32_f32_e32 v5, v5
	s_nop 0
	v_readfirstlane_b32 s24, v5
	s_mul_i32 s17, s17, s24
	s_mul_hi_u32 s17, s24, s17
	s_add_i32 s24, s24, s17
	s_mul_hi_u32 s17, s7, s24
	s_mul_i32 s24, s17, s4
	s_sub_i32 s7, s7, s24
	s_add_i32 s24, s17, 1
	s_sub_i32 s25, s7, s4
	s_cmp_ge_u32 s7, s4
	s_cselect_b32 s17, s24, s17
	s_cselect_b32 s7, s25, s7
	s_add_i32 s24, s17, 1
	s_cmp_ge_u32 s7, s4
	s_cselect_b32 s4, s24, s17
	s_xor_b32 s4, s4, s0
	s_sub_i32 s4, s4, s0
	s_sext_i32_i8 s0, s8
	v_cvt_f32_i32_e32 v5, s0
	s_mul_i32 s6, s4, s6
	s_sub_i32 s5, s5, s6
	v_cvt_f32_i32_e32 v7, s5
	v_rcp_iflag_f32_e32 v9, v5
	s_xor_b32 s0, s5, s0
	s_ashr_i32 s0, s0, 30
	s_or_b32 s0, s0, 1
	v_mul_f32_e32 v9, v7, v9
	v_trunc_f32_e32 v9, v9
	v_fma_f32 v7, -v9, v5, v7
	v_cvt_i32_f32_e32 v9, v9
	v_cmp_ge_f32_e64 s[6:7], |v7|, |v5|
	s_and_b64 s[6:7], s[6:7], exec
	s_cselect_b32 s0, s0, 0
	v_readfirstlane_b32 s6, v9
	s_add_i32 s6, s6, s0
	s_mul_i32 s7, s6, s8
	s_sub_i32 s8, s5, s7
	s_sext_i32_i8 s5, s8
	v_lshl_add_u32 v5, s5, 7, v12
	v_lshl_or_b32 v7, s5, 8, v13
	s_ashr_i32 s5, s4, 31
	s_sext_i32_i8 s0, s6
	s_lshl_b64 s[16:17], s[4:5], s16
	v_lshl_or_b32 v30, s0, 6, v14
	s_lshl_b64 s[16:17], s[16:17], 2
	v_ashrrev_i32_e32 v31, 31, v30
	s_add_u32 s16, s18, s16
	v_cndmask_b32_e32 v28, v5, v7, vcc
	s_addc_u32 s17, s15, s17
	v_lshlrev_b64 v[30:31], s19, v[30:31]
	v_lshl_add_u64 v[30:31], v[30:31], 2, s[16:17]
	v_ashrrev_i32_e32 v29, 31, v28
	v_lshl_add_u64 v[52:53], v[28:29], 2, v[30:31]
	s_lshl_b32 s0, s9, 2
	s_lshl_b64 s[16:17], 12, s19
	v_lshl_add_u64 v[36:37], v[52:53], 0, s[0:1]
	v_lshl_add_u64 v[44:45], v[52:53], 0, s[16:17]
	s_lshl_b64 s[16:17], 24, s19
	v_lshl_add_u64 v[54:55], v[36:37], 0, s[0:1]
	v_lshl_add_u64 v[56:57], v[52:53], 0, s[16:17]
	s_lshl_b64 s[16:17], 28, s19
	s_lshl_b32 s0, s9, 3
	v_lshl_add_u64 v[58:59], v[52:53], 0, s[16:17]
	v_lshl_add_u64 v[60:61], v[54:55], 0, s[0:1]
	s_lshl_b64 s[16:17], 20, s19
	global_load_dwordx4 v[28:31], v[52:53], off nt
	global_load_dwordx4 v[32:35], v[36:37], off nt
	s_nop 0
	global_load_dwordx4 v[36:39], v[54:55], off nt
	global_load_dwordx4 v[40:43], v[44:45], off nt
	s_nop 0
	global_load_dwordx4 v[44:47], v[56:57], off nt
	global_load_dwordx4 v[48:51], v[58:59], off nt
	v_lshl_add_u64 v[62:63], v[52:53], 0, s[16:17]
	global_load_dwordx4 v[52:55], v[60:61], off nt
	global_load_dwordx4 v[56:59], v[62:63], off nt
	s_lshl_b64 s[4:5], s[4:5], s19
	s_lshl_b64 s[4:5], s[4:5], 11
	s_add_u32 s0, s22, s4
	s_addc_u32 s9, s23, s5
	s_bfe_i64 s[4:5], s[8:9], 0x80000
	s_bfe_i64 s[6:7], s[6:7], 0x80000
	s_lshl_b64 s[4:5], s[4:5], 19
	s_add_u32 s0, s0, s4
	s_addc_u32 s8, s9, s5
	s_lshl_b64 s[4:5], s[6:7], 15
	s_add_u32 s4, s0, s4
	s_addc_u32 s5, s8, s5
	v_mov_b32_e32 v5, v3
	s_add_i32 s3, s3, -1
	s_cmp_eq_u32 s3, 0
	s_waitcnt vmcnt(7)
	ds_write_b128 v16, v[28:31]
	s_waitcnt vmcnt(6)
	ds_write2_b32 v17, v32, v33 offset1:1
	ds_write2_b32 v18, v34, v35 offset1:1
	s_waitcnt vmcnt(3)
	ds_write2_b64 v24, v[44:45], v[46:47] offset1:1
	s_waitcnt vmcnt(2)
	ds_write2_b32 v25, v48, v49 offset1:1
	ds_write2_b32 v26, v50, v51 offset1:1
	ds_write2_b64 v19, v[36:37], v[38:39] offset1:1
	ds_write2_b32 v20, v40, v41 offset1:1
	ds_write2_b32 v21, v42, v43 offset1:1
	s_waitcnt vmcnt(1)
	ds_write_b128 v16, v[52:55] offset:4112
	s_waitcnt vmcnt(0)
	ds_write2_b32 v22, v56, v57 offset1:1
	ds_write2_b32 v23, v58, v59 offset1:1
	s_waitcnt lgkmcnt(0)
	s_barrier
	ds_read_b32 v7, v27 offset:1028
	ds_read_b32 v9, v27 offset:3084
	ds_read_b32 v11, v27 offset:5140
	ds_read_b32 v31, v27 offset:7196
	ds_read_b32 v32, v27 offset:6168
	ds_read_b32 v30, v27 offset:4112
	ds_read_b32 v29, v27 offset:2056
	ds_read_b32 v28, v27
	s_waitcnt lgkmcnt(0)
	v_cvt_pk_bf16_f32 v28, v28, v7
	v_cvt_pk_bf16_f32 v29, v29, v9
	v_cvt_pk_bf16_f32 v30, v30, v11
	v_cvt_pk_bf16_f32 v31, v32, v31
	ds_read_b32 v7, v27 offset:1060
	ds_read_b32 v9, v27 offset:3116
	ds_read_b32 v11, v27 offset:5172
	ds_read_b32 v36, v27 offset:7228
	ds_read_b32 v37, v27 offset:6200
	ds_read_b32 v38, v27 offset:4144
	ds_read_b32 v39, v27 offset:2088
	ds_read_b32 v40, v27 offset:32
	v_lshl_add_u64 v[32:33], s[4:5], 0, v[2:3]
	v_lshl_add_u64 v[34:35], v[32:33], 0, v[4:5]
	global_store_dwordx4 v[34:35], v[28:31], off
	s_cselect_b64 s[4:5], -1, 0
	s_waitcnt lgkmcnt(0)
	v_cvt_pk_bf16_f32 v28, v40, v7
	v_cvt_pk_bf16_f32 v29, v39, v9
	v_cvt_pk_bf16_f32 v30, v38, v11
	v_cvt_pk_bf16_f32 v31, v37, v36
	ds_read_b32 v5, v27 offset:1092
	ds_read_b32 v9, v27 offset:3148
	ds_read_b32 v11, v27 offset:5204
	ds_read_b32 v36, v27 offset:6232
	ds_read_b32 v37, v27 offset:4176
	ds_read_b32 v38, v27 offset:2120
	ds_read_b32 v39, v27 offset:64
	ds_read_b32 v40, v27 offset:7260
	v_mov_b32_e32 v7, v3
	v_lshl_add_u64 v[34:35], v[32:33], 0, v[6:7]
	global_store_dwordx4 v[34:35], v[28:31], off
	s_waitcnt lgkmcnt(1)
	s_nop 0
	v_cvt_pk_bf16_f32 v28, v39, v5
	v_cvt_pk_bf16_f32 v29, v38, v9
	v_cvt_pk_bf16_f32 v30, v37, v11
	s_waitcnt lgkmcnt(0)
	v_cvt_pk_bf16_f32 v31, v36, v40
	ds_read_b32 v5, v27 offset:1124
	ds_read_b32 v7, v27 offset:3180
	ds_read_b32 v11, v27 offset:5236
	ds_read_b32 v36, v27 offset:6264
	ds_read_b32 v37, v27 offset:4208
	ds_read_b32 v38, v27 offset:2152
	ds_read_b32 v39, v27 offset:96
	ds_read_b32 v40, v27 offset:7292
	v_mov_b32_e32 v9, v3
	v_lshl_add_u64 v[34:35], v[32:33], 0, v[8:9]
	global_store_dwordx4 v[34:35], v[28:31], off
	s_waitcnt lgkmcnt(1)
	s_nop 0
	v_cvt_pk_bf16_f32 v28, v39, v5
	v_cvt_pk_bf16_f32 v29, v38, v7
	v_cvt_pk_bf16_f32 v30, v37, v11
	v_mov_b32_e32 v11, v3
	v_lshl_add_u64 v[32:33], v[32:33], 0, v[10:11]
	s_waitcnt lgkmcnt(0)
	v_cvt_pk_bf16_f32 v31, v36, v40
	global_store_dwordx4 v[32:33], v[28:31], off
	s_branch .LBB0_2279
